# conv phase rebalanced: each CU does 2 latent tiles + one 8-position chunk of a context tile (was: 32 CUs doing a whole third tile)
# baseline (speedup 1.0000x reference)
; #define GAS __attribute__((address_space(1)))
; #define LAS __attribute__((address_space(3)))
; template <class T> __device__ __forceinline__ T* wsp(const Frame& F, size_t off) { return (T*)(F.ws + off); }
; #define NTLD(P) (NT_STREAMS ? __builtin_nontemporal_load(P) : *(P))
; __device__ __forceinline__ void phase_conv(Frame& F) {
;     const int c = F.tid;
;     float w[31];
; #pragma unroll
;     for (int j = 0; j < 31; ++j) w[j] = inp(F, I_CONVW)[j * 512 + c];
;     const float bias = inp(F, I_CONVB)[c], lg = inp(F, I_LNG)[c], lb = inp(F, I_LNB)[c];
;     LAS bf16* tile = (LAS bf16*)(F.lds);
;     const bf16* AG = wsp<const bf16>(F, WS_AGLU); bf16* MIX = wsp<bf16>(F, WS_XA);
;     for (int ti = F.vcu; ti < 544; ti += F.G) {
;         int rowbase, L, p0;
;         if (ti < 512) { rowbase = (ti >> 6) * SEQ; p0 = (ti & 63) * 64; L = SEQ; } else { const int q = ti - 512; rowbase = TL + (q >> 2) * CTXL; p0 = (q & 3) * 64; L = CTXL; }
;         __syncthreads();
;         for (int rr = F.wave; rr < 94; rr += 8) { const int p = p0 - 15 + rr; v4u val = (v4u){0u, 0u, 0u, 0u};
;             if (p >= 0 && p < L) val = NTLD((const GAS v4u*)(AG + (size_t)(rowbase + p) * 512 + F.lane * 8));
;             *(LAS v4u*)(tile + rr * 512 + F.lane * 8) = val; }
;         __syncthreads();
.LBB0_342:
	s_cmp_lt_i32 s34, 4
	s_cselect_b64 s[40:41], -1, 0
	s_and_b64 s[0:1], s[40:41], s[2:3]
	s_andn2_b64 vcc, exec, s[0:1]
	s_cbranch_vccnz .LBB0_439
	s_add_i32 s0, 0, 0x20240
	v_mov_b32_e32 v2, v0
	s_mov_b64 s[20:21], s[38:39]
	s_add_i32 s1, 0, 0x20250
	v_mov_b32_e32 v1, s0
	ds_read_b128 v[4:7], v1
	v_mov_b32_e32 v1, s1
	ds_read_b128 v[8:11], v1
	s_cmpk_gt_i32 s71, 0x21f
	v_readfirstlane_b32 s9, v2
	s_waitcnt lgkmcnt(0)
	v_readfirstlane_b32 s10, v4
	v_readfirstlane_b32 s11, v5
	v_readfirstlane_b32 s4, v6
	v_readfirstlane_b32 s5, v7
	v_readfirstlane_b32 s2, v8
	v_readfirstlane_b32 s3, v9
	v_readfirstlane_b32 s0, v10
	v_readfirstlane_b32 s1, v11
	s_cbranch_scc1 .LBB0_355
	v_ashrrev_i32_e32 v3, 31, v2
	v_lshlrev_b64 v[4:5], 2, v[2:3]
	v_lshl_add_u64 v[12:13], s[10:11], 0, v[4:5]
	v_add_co_u32_e32 v6, vcc, 0x1000, v12
	v_lshl_add_u32 v69, v2, 1, 0
	s_nop 0
	v_addc_co_u32_e32 v7, vcc, 0, v13, vcc
	v_add_co_u32_e32 v8, vcc, 0x2000, v12
	s_movk_i32 s23, 0x2000
	s_nop 0
	v_addc_co_u32_e32 v9, vcc, 0, v13, vcc
	v_add_co_u32_e32 v10, vcc, 0x3000, v12
	s_movk_i32 s42, 0x3000
	s_nop 0
	v_addc_co_u32_e32 v11, vcc, 0, v13, vcc
	global_load_dword v1, v[12:13], off
	global_load_dword v48, v[12:13], off offset:2048
	global_load_dword v49, v[6:7], off
	global_load_dword v50, v[6:7], off offset:2048
	global_load_dword v51, v[8:9], off
	global_load_dword v52, v[8:9], off offset:2048
	global_load_dword v53, v[10:11], off
	global_load_dword v54, v[10:11], off offset:2048
	v_add_co_u32_e32 v6, vcc, 0x4000, v12
	s_movk_i32 s43, 0x4000
	s_nop 0
	v_addc_co_u32_e32 v7, vcc, 0, v13, vcc
	v_add_co_u32_e32 v8, vcc, 0x5000, v12
	s_movk_i32 s45, 0xfc0
	s_nop 0
	v_addc_co_u32_e32 v9, vcc, 0, v13, vcc
	v_add_co_u32_e32 v10, vcc, 0x6000, v12
	s_movk_i32 s46, 0x100
	s_nop 0
	v_addc_co_u32_e32 v11, vcc, 0, v13, vcc
	v_add_co_u32_e32 v14, vcc, 0x7000, v12
	s_mov_b32 s22, 0x3c800000
	s_nop 0
	v_addc_co_u32_e32 v15, vcc, 0, v13, vcc
	global_load_dword v55, v[6:7], off
	global_load_dword v56, v[6:7], off offset:2048
	global_load_dword v57, v[8:9], off
	global_load_dword v58, v[8:9], off offset:2048
	global_load_dword v59, v[10:11], off
	global_load_dword v60, v[10:11], off offset:2048
	global_load_dword v61, v[14:15], off
	global_load_dword v62, v[14:15], off offset:2048
	v_add_co_u32_e32 v14, vcc, 0x8000, v12
	s_mov_b32 s47, 0x800000
	s_nop 0
	v_addc_co_u32_e32 v15, vcc, 0, v13, vcc
	v_add_co_u32_e32 v16, vcc, 0x9000, v12
	s_movk_i32 s48, 0x7fff
	s_nop 0
	v_addc_co_u32_e32 v17, vcc, 0, v13, vcc
	v_add_co_u32_e32 v18, vcc, 0xa000, v12
	v_mov_b32_e32 v77, 0xc00
	s_nop 0
	v_addc_co_u32_e32 v19, vcc, 0, v13, vcc
	v_add_co_u32_e32 v20, vcc, 0xb000, v12
	s_mov_b32 s49, s71
	s_mov_b32 s98, 0x30000
	s_mov_b32 s99, 0
	s_mov_b32 s100, 0
	s_mov_b32 s101, 0
	s_nop 0
	v_addc_co_u32_e32 v21, vcc, 0, v13, vcc
	global_load_dword v63, v[14:15], off
	global_load_dword v64, v[14:15], off offset:2048
	global_load_dword v65, v[16:17], off
	global_load_dword v6, v[16:17], off offset:2048
	global_load_dword v7, v[18:19], off
	global_load_dword v8, v[18:19], off offset:2048
	global_load_dword v9, v[20:21], off
	global_load_dword v10, v[20:21], off offset:2048
	v_add_co_u32_e32 v18, vcc, 0xc000, v12
	s_nop 1
	v_addc_co_u32_e32 v19, vcc, 0, v13, vcc
	v_add_co_u32_e32 v20, vcc, 0xd000, v12
	s_nop 1
	v_addc_co_u32_e32 v21, vcc, 0, v13, vcc
	v_add_co_u32_e32 v22, vcc, 0xe000, v12
	s_nop 1
	v_addc_co_u32_e32 v23, vcc, 0, v13, vcc
	v_add_co_u32_e32 v24, vcc, 0xf000, v12
	s_nop 1
	v_addc_co_u32_e32 v25, vcc, 0, v13, vcc
	global_load_dword v11, v[18:19], off
	global_load_dword v12, v[18:19], off offset:2048
	global_load_dword v13, v[20:21], off
	global_load_dword v14, v[20:21], off offset:2048
	global_load_dword v15, v[22:23], off
	global_load_dword v16, v[22:23], off offset:2048
	global_load_dword v17, v[24:25], off
	v_lshl_add_u64 v[18:19], s[4:5], 0, v[4:5]
	global_load_dword v66, v[18:19], off
	v_lshl_add_u64 v[18:19], s[2:3], 0, v[4:5]
	v_lshl_add_u64 v[4:5], s[0:1], 0, v[4:5]
	global_load_dword v67, v[18:19], off
	global_load_dword v68, v[4:5], off
	v_mbcnt_lo_u32_b32 v4, -1, 0
	v_mbcnt_hi_u32_b32 v4, -1, v4
	v_and_b32_e32 v5, 64, v4
	v_add_u32_e32 v5, 64, v5
	v_xor_b32_e32 v18, 1, v4
	v_cmp_lt_i32_e32 vcc, v18, v5
	s_ashr_i32 s2, s9, 6
	s_cmpk_gt_i32 s2, 0x5d
	v_cndmask_b32_e32 v18, v4, v18, vcc
	v_lshlrev_b32_e32 v70, 2, v18
	v_xor_b32_e32 v18, 2, v4
	v_cmp_lt_i32_e32 vcc, v18, v5
	s_mov_b64 s[0:1], 0xec00000
	s_cselect_b64 s[18:19], -1, 0
	v_cndmask_b32_e32 v18, v4, v18, vcc
	v_lshlrev_b32_e32 v71, 2, v18
	v_xor_b32_e32 v18, 4, v4
	v_cmp_lt_i32_e32 vcc, v18, v5
	s_movk_i32 s9, 0x1000
	s_add_i32 s44, s2, -15
	v_cndmask_b32_e32 v18, v4, v18, vcc
	v_lshlrev_b32_e32 v72, 2, v18
	v_xor_b32_e32 v18, 8, v4
	v_cmp_lt_i32_e32 vcc, v18, v5
	s_nop 1
	v_cndmask_b32_e32 v18, v4, v18, vcc
	v_lshlrev_b32_e32 v73, 2, v18
	v_xor_b32_e32 v18, 16, v4
	v_cmp_lt_i32_e32 vcc, v18, v5
	s_nop 1
	v_cndmask_b32_e32 v18, v4, v18, vcc
	v_lshlrev_b32_e32 v74, 2, v18
	v_xor_b32_e32 v18, 32, v4
	v_cmp_lt_i32_e32 vcc, v18, v5
	v_mov_b32_e32 v5, 0
	s_nop 0
	v_cndmask_b32_e32 v4, v4, v18, vcc
	v_lshlrev_b32_e32 v75, 2, v4
	v_lshlrev_b32_e32 v4, 4, v2
	v_and_b32_e32 v4, 0x3f0, v4
	v_lshl_add_u64 v[18:19], s[20:21], 0, v[4:5]
	v_lshl_add_u64 v[18:19], v[18:19], 0, s[0:1]
	s_lshl_b32 s0, s2, 10
	s_add_i32 s0, s0, 0
	v_add_u32_e32 v76, s0, v4
	v_lshl_add_u64 v[2:3], v[2:3], 1, s[20:21]
	s_mov_b64 s[0:1], 0x13200000
	v_lshl_add_u64 v[20:21], v[2:3], 0, s[0:1]

; __device__ __forceinline__ void phase_conv(Frame& F) {
;     ...
;         for (int ch = 0; ch < 8; ++ch) {
;             float in[38];
; #pragma unroll
;             for (int i = 0; i < 38; ++i) in[i] = bf2f(tile[(ch * 8 + i) * 512 + c]);
;             float a[8], s[8], ss[8];
; #pragma unroll
;             for (int q = 0; q < 8; ++q) { float t = bias;
; #pragma unroll
;                 for (int j = 0; j < 31; ++j) t += w[j] * in[q + j];
;                 a[q] = t; s[q] = t; ss[q] = t * t; }
.LBB0_352:
	v_mad_i64_i32 v[2:3], s[0:1], s5, v77, v[20:21]
	s_mov_b32 s38, s99
	s_mov_b32 s39, 0
	v_add_u32_e32 v100, s100, v69
	s_waitcnt lgkmcnt(0)
	s_barrier
.LBB0_353:
	ds_read_u16 v32, v100 offset:2048
	ds_read_u16 v33, v100 offset:3072
	ds_read_u16 v34, v100 offset:4096
	ds_read_u16 v35, v100 offset:5120
	ds_read_u16 v36, v100 offset:6144
	ds_read_u16 v37, v100 offset:7168
	ds_read_u16 v38, v100 offset:8192
	ds_read_u16 v39, v100 offset:9216
	ds_read_u16 v40, v100 offset:10240
	ds_read_u16 v41, v100 offset:11264
	ds_read_u16 v42, v100 offset:12288
	ds_read_u16 v43, v100 offset:13312
	ds_read_u16 v44, v100 offset:14336
	ds_read_u16 v45, v100 offset:15360
	ds_read_u16 v46, v100 offset:16384
	ds_read_u16 v47, v100 offset:17408
	ds_read_u16 v82, v100 offset:18432
	ds_read_u16 v78, v100 offset:19456
	ds_read_u16 v85, v100 offset:20480
	ds_read_u16 v79, v100 offset:21504
	ds_read_u16 v86, v100 offset:22528
	ds_read_u16 v80, v100 offset:23552
	ds_read_u16 v87, v100 offset:24576
	ds_read_u16 v81, v100 offset:25600
	ds_read_u16 v88, v100 offset:26624
	ds_read_u16 v83, v100 offset:27648
	ds_read_u16 v84, v100 offset:28672
	ds_read_u16 v97, v100 offset:29696
	ds_read_u16 v89, v100 offset:30720
	ds_read_u16 v90, v100 offset:31744
	ds_read_u16 v98, v100
	ds_read_u16 v99, v100 offset:1024
	ds_read_u16 v91, v100 offset:32768
	ds_read_u16 v95, v100 offset:33792
	ds_read_u16 v92, v100 offset:34816
	ds_read_u16 v96, v100 offset:35840
	ds_read_u16 v93, v100 offset:36864
	ds_read_u16 v94, v100 offset:37888
	s_waitcnt lgkmcnt(7)
	v_lshlrev_b32_e32 v101, 16, v98
	s_waitcnt lgkmcnt(6)
	v_lshlrev_b32_e32 v140, 16, v99
	v_lshlrev_b32_e32 v168, 16, v32
	v_lshlrev_b32_e32 v169, 16, v33
	v_lshlrev_b32_e32 v170, 16, v34
	v_lshlrev_b32_e32 v171, 16, v35
	v_lshlrev_b32_e32 v172, 16, v36
	v_lshlrev_b32_e32 v173, 16, v37
	v_lshlrev_b32_e32 v178, 16, v42
	v_lshlrev_b32_e32 v179, 16, v43
	v_lshlrev_b32_e32 v98, 16, v78
	v_lshlrev_b32_e32 v103, 16, v86
	v_lshlrev_b32_e32 v102, 16, v79
	v_lshlrev_b32_e32 v79, 16, v87
	v_lshlrev_b32_e32 v78, 16, v80
	v_lshlrev_b32_e32 v87, 16, v88
	v_lshlrev_b32_e32 v86, 16, v81
	v_lshlrev_b32_e32 v42, 16, v83
	v_lshlrev_b32_e32 v43, 16, v84
	v_fma_f32 v101, v1, v101, v66
	v_lshlrev_b32_e32 v174, 16, v38
	v_lshlrev_b32_e32 v180, 16, v44
	v_lshlrev_b32_e32 v181, 16, v45
	v_pk_mul_f32 v[44:45], v[12:13], v[86:87]
	v_fma_f32 v185, v1, v140, v66
	v_pk_mov_b32 v[108:109], v[78:79], v[86:87] op_sel:[1,0]
	v_pk_mov_b32 v[110:111], v[86:87], v[42:43] op_sel:[1,0]
	v_fma_f32 v186, v1, v168, v66
	v_pk_mul_f32 v[118:119], v[10:11], v[86:87]
	v_fma_f32 v187, v1, v169, v66
	v_fma_f32 v188, v1, v170, v66
	v_pk_mul_f32 v[126:127], v[8:9], v[86:87]
	v_fma_f32 v189, v1, v171, v66
	v_fma_f32 v190, v1, v172, v66
	v_pk_mul_f32 v[134:135], v[6:7], v[86:87]
	v_fma_f32 v87, v1, v173, v66
	v_fmac_f32_e32 v101, v48, v140
	v_lshlrev_b32_e32 v175, 16, v39
	v_fmac_f32_e32 v185, v48, v168
	v_fmac_f32_e32 v186, v48, v169
	v_fmac_f32_e32 v187, v48, v170
	v_fmac_f32_e32 v188, v48, v171
	v_fmac_f32_e32 v189, v48, v172
	v_fmac_f32_e32 v190, v48, v173
	v_fmac_f32_e32 v87, v48, v174
	v_fmac_f32_e32 v101, v49, v168
	v_lshlrev_b32_e32 v176, 16, v40
	v_fmac_f32_e32 v185, v49, v169
	v_fmac_f32_e32 v186, v49, v170
	v_fmac_f32_e32 v187, v49, v171
	v_fmac_f32_e32 v188, v49, v172
	v_fmac_f32_e32 v189, v49, v173
	v_fmac_f32_e32 v190, v49, v174
	v_fmac_f32_e32 v87, v49, v175
	v_fmac_f32_e32 v101, v50, v169
	v_lshlrev_b32_e32 v177, 16, v41
	v_fmac_f32_e32 v185, v50, v170
	v_fmac_f32_e32 v186, v50, v171
	v_fmac_f32_e32 v187, v50, v172
	v_fmac_f32_e32 v188, v50, v173
	v_fmac_f32_e32 v189, v50, v174
	v_fmac_f32_e32 v190, v50, v175
	v_fmac_f32_e32 v87, v50, v176
	v_fmac_f32_e32 v101, v51, v170
	v_fmac_f32_e32 v185, v51, v171
	v_fmac_f32_e32 v186, v51, v172
	v_fmac_f32_e32 v187, v51, v173
	v_fmac_f32_e32 v188, v51, v174
	v_fmac_f32_e32 v189, v51, v175
	v_fmac_f32_e32 v190, v51, v176
	v_fmac_f32_e32 v87, v51, v177
	v_fmac_f32_e32 v101, v52, v171
	v_fmac_f32_e32 v185, v52, v172
	v_fmac_f32_e32 v186, v52, v173
	v_fmac_f32_e32 v187, v52, v174
	v_fmac_f32_e32 v188, v52, v175
	v_fmac_f32_e32 v189, v52, v176
	v_fmac_f32_e32 v190, v52, v177
	v_fmac_f32_e32 v87, v52, v178
	v_fmac_f32_e32 v101, v53, v172
	v_fmac_f32_e32 v185, v53, v173
	v_fmac_f32_e32 v186, v53, v174
	v_fmac_f32_e32 v187, v53, v175
	v_fmac_f32_e32 v188, v53, v176
	v_fmac_f32_e32 v189, v53, v177
	v_fmac_f32_e32 v190, v53, v178
	v_fmac_f32_e32 v87, v53, v179
	v_fmac_f32_e32 v101, v54, v173
	v_fmac_f32_e32 v185, v54, v174
	v_fmac_f32_e32 v186, v54, v175
	v_fmac_f32_e32 v187, v54, v176
	v_fmac_f32_e32 v188, v54, v177
	v_fmac_f32_e32 v189, v54, v178
	v_fmac_f32_e32 v190, v54, v179
	v_fmac_f32_e32 v87, v54, v180
	v_fmac_f32_e32 v101, v55, v174
	v_lshlrev_b32_e32 v182, 16, v46
	v_fmac_f32_e32 v185, v55, v175
	v_fmac_f32_e32 v186, v55, v176
	v_fmac_f32_e32 v187, v55, v177
	v_fmac_f32_e32 v188, v55, v178
	v_fmac_f32_e32 v189, v55, v179
	v_fmac_f32_e32 v190, v55, v180
	v_fmac_f32_e32 v87, v55, v181
	v_fmac_f32_e32 v101, v56, v175
	v_lshlrev_b32_e32 v183, 16, v47
	v_fmac_f32_e32 v185, v56, v176
	v_fmac_f32_e32 v186, v56, v177
	v_fmac_f32_e32 v187, v56, v178
	v_fmac_f32_e32 v188, v56, v179
	v_fmac_f32_e32 v189, v56, v180
	v_fmac_f32_e32 v190, v56, v181
	v_fmac_f32_e32 v87, v56, v182
	v_fmac_f32_e32 v101, v57, v176
	v_lshlrev_b32_e32 v184, 16, v82
	v_fmac_f32_e32 v185, v57, v177
	v_fmac_f32_e32 v186, v57, v178
	v_fmac_f32_e32 v187, v57, v179
	v_fmac_f32_e32 v188, v57, v180
	v_fmac_f32_e32 v189, v57, v181
	v_fmac_f32_e32 v190, v57, v182
	v_fmac_f32_e32 v87, v57, v183
	v_fmac_f32_e32 v101, v58, v177
	v_fmac_f32_e32 v185, v58, v178
; __device__ __forceinline__ void phase_conv(Frame& F) {
;     ...
;             for (int q = 0; q < 8; ++q) { float t = bias;
; #pragma unroll
;                 for (int j = 0; j < 31; ++j) t += w[j] * in[q + j];
;                 a[q] = t; s[q] = t; ss[q] = t * t; }
	v_fmac_f32_e32 v186, v58, v179
	v_fmac_f32_e32 v187, v58, v180
	v_fmac_f32_e32 v188, v58, v181
	v_fmac_f32_e32 v189, v58, v182
	v_fmac_f32_e32 v190, v58, v183
	v_fmac_f32_e32 v87, v58, v184
	v_fmac_f32_e32 v101, v59, v178
	v_lshlrev_b32_e32 v99, 16, v85
	v_fmac_f32_e32 v185, v59, v179
	v_fmac_f32_e32 v186, v59, v180
	v_fmac_f32_e32 v187, v59, v181
	v_fmac_f32_e32 v188, v59, v182
	v_fmac_f32_e32 v189, v59, v183
	v_fmac_f32_e32 v190, v59, v184
	v_fmac_f32_e32 v87, v59, v98
	v_fmac_f32_e32 v101, v60, v179
	v_fmac_f32_e32 v185, v60, v180
	v_fmac_f32_e32 v186, v60, v181
	v_fmac_f32_e32 v187, v60, v182
	v_fmac_f32_e32 v188, v60, v183
	v_fmac_f32_e32 v189, v60, v184
	v_fmac_f32_e32 v190, v60, v98
	v_fmac_f32_e32 v87, v60, v99
	v_fmac_f32_e32 v101, v61, v180
	v_fmac_f32_e32 v185, v61, v181
	v_fmac_f32_e32 v186, v61, v182
	v_fmac_f32_e32 v187, v61, v183
	v_fmac_f32_e32 v188, v61, v184
	v_fmac_f32_e32 v189, v61, v98
	v_fmac_f32_e32 v190, v61, v99
	v_fmac_f32_e32 v87, v61, v102
	v_fmac_f32_e32 v101, v62, v181
	v_fmac_f32_e32 v185, v62, v182
	v_fmac_f32_e32 v186, v62, v183
	v_fmac_f32_e32 v187, v62, v184
	v_fmac_f32_e32 v188, v62, v98
	v_fmac_f32_e32 v189, v62, v99
	v_fmac_f32_e32 v190, v62, v102
	v_fmac_f32_e32 v87, v62, v103
	v_fmac_f32_e32 v101, v63, v182
	v_fmac_f32_e32 v185, v63, v183
	v_fmac_f32_e32 v186, v63, v184
	v_fmac_f32_e32 v187, v63, v98
	v_fmac_f32_e32 v188, v63, v99
	v_fmac_f32_e32 v189, v63, v102
	v_fmac_f32_e32 v190, v63, v103
	v_fmac_f32_e32 v87, v63, v78
	v_fmac_f32_e32 v101, v64, v183
	v_lshlrev_b32_e32 v81, 16, v90
	v_lshlrev_b32_e32 v80, 16, v89
	s_waitcnt lgkmcnt(4)
	v_lshlrev_b32_e32 v83, 16, v95
	v_lshlrev_b32_e32 v82, 16, v91
	s_waitcnt lgkmcnt(2)
	v_lshlrev_b32_e32 v85, 16, v96
	v_lshlrev_b32_e32 v84, 16, v92
	s_waitcnt lgkmcnt(1)
	v_lshlrev_b32_e32 v88, 16, v93
	s_waitcnt lgkmcnt(0)
	v_lshlrev_b32_e32 v89, 16, v94
	v_pk_mul_f32 v[90:91], v[6:7], v[98:99]
	v_pk_mov_b32 v[104:105], v[98:99], v[102:103] op_sel:[1,0]
	v_pk_mov_b32 v[106:107], v[102:103], v[78:79] op_sel:[1,0]
	v_fmac_f32_e32 v185, v64, v184
	v_fmac_f32_e32 v186, v64, v98
	v_fmac_f32_e32 v187, v64, v99
	v_fmac_f32_e32 v188, v64, v102
	v_fmac_f32_e32 v189, v64, v103
	v_fmac_f32_e32 v190, v64, v78
	v_fmac_f32_e32 v87, v64, v79
	v_fmac_f32_e32 v101, v65, v184
	v_pk_mul_f32 v[94:95], v[10:11], v[78:79]
	v_pk_mul_f32 v[36:37], v[14:15], v[42:43]
	v_mov_b32_e32 v96, v43
	v_pk_mul_f32 v[114:115], v[6:7], v[102:103]
	v_pk_mul_f32 v[116:117], v[8:9], v[78:79]
	v_pk_mul_f32 v[120:121], v[12:13], v[42:43]
	v_pk_mul_f32 v[124:125], v[6:7], v[78:79]
	v_pk_mul_f32 v[128:129], v[10:11], v[42:43]
	v_pk_mov_b32 v[132:133], v[82:83], v[84:85] op_sel:[1,0]
	v_pk_mul_f32 v[38:39], v[16:17], v[84:85]
	v_pk_mul_f32 v[136:137], v[8:9], v[42:43]
	v_pk_mul_f32 v[138:139], v[14:15], v[84:85]
	v_pk_mov_b32 v[84:85], v[84:85], v[88:89] op_sel:[1,0]
	v_pk_mul_f32 v[42:43], v[16:17], v[88:89]
	v_pk_mul_f32 v[88:89], v[6:7], v[104:105]
	v_pk_mul_f32 v[104:105], v[8:9], v[106:107]
	v_pk_mul_f32 v[140:141], v[10:11], v[108:109]
	v_pk_mul_f32 v[142:143], v[12:13], v[110:111]
	v_pk_mul_f32 v[106:107], v[6:7], v[106:107]
	v_pk_mul_f32 v[150:151], v[8:9], v[108:109]
	v_pk_mul_f32 v[152:153], v[10:11], v[110:111]
	v_pk_mul_f32 v[108:109], v[6:7], v[108:109]
	v_pk_mul_f32 v[162:163], v[8:9], v[110:111]
	v_pk_mul_f32 v[110:111], v[6:7], v[110:111]
	v_fmac_f32_e32 v185, v65, v98
	v_fmac_f32_e32 v186, v65, v99
	v_fmac_f32_e32 v187, v65, v102
	v_fmac_f32_e32 v188, v65, v103
	v_fmac_f32_e32 v189, v65, v78
	v_fmac_f32_e32 v190, v65, v79
	v_fmac_f32_e32 v87, v65, v86
	v_add_f32_e32 v78, v101, v90
	v_lshlrev_b32_e32 v97, 16, v97
	v_pk_mul_f32 v[92:93], v[8:9], v[102:103]
	v_add_f32_e32 v79, v185, v88
	v_add_f32_e32 v86, v186, v114
	v_add_f32_e32 v88, v187, v106
	v_add_f32_e32 v90, v188, v124
	v_add_f32_e32 v98, v189, v108
	v_add_f32_e32 v99, v190, v134
	v_add_f32_e32 v87, v87, v110
	v_add_f32_e32 v78, v78, v91
	v_mov_b32_e32 v112, v97
	v_pk_mul_f32 v[144:145], v[14:15], v[96:97]
	v_pk_mul_f32 v[154:155], v[12:13], v[96:97]
	v_pk_mul_f32 v[164:165], v[10:11], v[96:97]
	v_pk_mul_f32 v[96:97], v[8:9], v[96:97]
	v_add_f32_e32 v79, v79, v89
	v_add_f32_e32 v86, v86, v115
	v_add_f32_e32 v88, v88, v107
	v_add_f32_e32 v89, v90, v125
	v_add_f32_e32 v90, v98, v109
	v_add_f32_e32 v91, v99, v135
	v_add_f32_e32 v87, v87, v111
	v_add_f32_e32 v78, v78, v92
	v_mov_b32_e32 v113, v80
	v_add_f32_e32 v79, v79, v104
	v_add_f32_e32 v86, v86, v116
	v_add_f32_e32 v88, v88, v150
	v_add_f32_e32 v89, v89, v126
	v_add_f32_e32 v90, v90, v162
	v_add_f32_e32 v91, v91, v136
	v_add_f32_e32 v87, v87, v96
	v_add_f32_e32 v78, v78, v93
	v_pk_mul_f32 v[32:33], v[16:17], v[80:81]
	v_pk_mul_f32 v[40:41], v[14:15], v[80:81]
	v_pk_mov_b32 v[122:123], v[80:81], v[82:83] op_sel:[1,0]
	v_pk_mul_f32 v[130:131], v[12:13], v[80:81]
	v_pk_mul_f32 v[80:81], v[10:11], v[80:81]
	v_pk_mul_f32 v[146:147], v[16:17], v[112:113]
	v_pk_mul_f32 v[148:149], v[14:15], v[112:113]
	v_pk_mul_f32 v[158:159], v[12:13], v[112:113]
	v_pk_mul_f32 v[112:113], v[10:11], v[112:113]
	v_add_f32_e32 v79, v79, v105
	v_add_f32_e32 v86, v86, v117
	v_add_f32_e32 v88, v88, v151
	v_add_f32_e32 v89, v89, v127
	v_add_f32_e32 v90, v90, v163
	v_add_f32_e32 v91, v91, v137
	v_add_f32_e32 v87, v87, v97
	v_add_f32_e32 v78, v78, v94
	v_add_f32_e32 v79, v79, v140
	v_add_f32_e32 v86, v86, v118
	v_add_f32_e32 v88, v88, v152
	v_add_f32_e32 v89, v89, v128
	v_add_f32_e32 v90, v90, v164
	v_add_f32_e32 v91, v91, v112
	v_add_f32_e32 v80, v87, v80
	v_add_f32_e32 v78, v78, v95
	v_pk_mul_f32 v[34:35], v[16:17], v[82:83]
	v_pk_mul_f32 v[46:47], v[14:15], v[82:83]
	v_pk_mul_f32 v[82:83], v[12:13], v[82:83]
; __device__ __forceinline__ void phase_conv(Frame& F) {
;     ...
;             for (int q = 0; q < 8; ++q) { float t = bias;
; #pragma unroll
;                 for (int j = 0; j < 31; ++j) t += w[j] * in[q + j];
;                 a[q] = t; s[q] = t; ss[q] = t * t; }
; #pragma unroll
;             for (int o = 1; o < 64; o <<= 1) {
;                 float ts[8], tq[8];
; #pragma unroll
;                 for (int q = 0; q < 8; ++q) { ts[q] = __shfl_xor(s[q], o); tq[q] = __shfl_xor(ss[q], o); }
; #pragma unroll
;                 for (int q = 0; q < 8; ++q) { s[q] += ts[q]; ss[q] += tq[q]; } }
	v_pk_mul_f32 v[156:157], v[16:17], v[122:123]
	v_pk_mul_f32 v[160:161], v[14:15], v[122:123]
	v_pk_mul_f32 v[122:123], v[12:13], v[122:123]
	v_add_f32_e32 v79, v79, v141
	v_add_f32_e32 v86, v86, v119
	v_add_f32_e32 v87, v88, v153
	v_add_f32_e32 v88, v89, v129
	v_add_f32_e32 v89, v90, v165
	v_add_f32_e32 v90, v91, v113
	v_add_f32_e32 v80, v80, v81
	v_add_f32_e32 v44, v78, v44
	v_add_f32_e32 v78, v79, v142
	v_add_f32_e32 v79, v86, v120
	v_add_f32_e32 v81, v87, v154
	v_add_f32_e32 v86, v88, v158
	v_add_f32_e32 v87, v89, v130
	v_add_f32_e32 v88, v90, v122
	v_add_f32_e32 v80, v80, v82
	v_add_f32_e32 v44, v44, v45
	v_pk_mul_f32 v[166:167], v[16:17], v[132:133]
	v_pk_mul_f32 v[132:133], v[14:15], v[132:133]
	v_add_f32_e32 v45, v78, v143
	v_add_f32_e32 v78, v79, v121
	v_add_f32_e32 v79, v81, v155
	v_add_f32_e32 v81, v86, v159
	v_add_f32_e32 v82, v87, v131
	v_add_f32_e32 v86, v88, v123
	v_add_f32_e32 v80, v80, v83
	v_add_f32_e32 v36, v44, v36
	v_add_f32_e32 v44, v45, v144
	v_add_f32_e32 v45, v78, v148
	v_add_f32_e32 v40, v79, v40
	v_add_f32_e32 v78, v81, v160
	v_add_f32_e32 v46, v82, v46
	v_add_f32_e32 v79, v86, v132
	v_add_f32_e32 v80, v80, v138
	v_add_f32_e32 v36, v36, v37
	v_pk_mul_f32 v[84:85], v[16:17], v[84:85]
	v_add_f32_e32 v37, v44, v145
	v_add_f32_e32 v44, v45, v149
	v_add_f32_e32 v40, v40, v41
	v_add_f32_e32 v41, v78, v161
	v_add_f32_e32 v45, v46, v47
	v_add_f32_e32 v46, v79, v133
	v_add_f32_e32 v47, v80, v139
	v_add_f32_e32 v36, v36, v146
	v_add_f32_e32 v32, v37, v32
	v_add_f32_e32 v44, v44, v156
	v_add_f32_e32 v34, v40, v34
	v_add_f32_e32 v40, v41, v166
	v_add_f32_e32 v38, v45, v38
	v_add_f32_e32 v46, v46, v84
	v_add_f32_e32 v42, v47, v42
	v_add_f32_e32 v37, v36, v147
	v_add_f32_e32 v33, v32, v33
	v_add_f32_e32 v41, v44, v157
	v_add_f32_e32 v35, v34, v35
	v_add_f32_e32 v45, v40, v167
	v_add_f32_e32 v39, v38, v39
	v_add_f32_e32 v47, v46, v85
	v_add_f32_e32 v43, v42, v43
	v_mul_f32_e32 v36, v37, v37
	ds_bpermute_b32 v79, v70, v37
	v_mul_f32_e32 v32, v33, v33
	v_mul_f32_e32 v40, v41, v41
	v_mul_f32_e32 v34, v35, v35
	v_mul_f32_e32 v44, v45, v45
	v_mul_f32_e32 v38, v39, v39
	v_mul_f32_e32 v46, v47, v47
	v_mul_f32_e32 v42, v43, v43
	ds_bpermute_b32 v78, v70, v36
	ds_bpermute_b32 v81, v70, v33
	ds_bpermute_b32 v83, v70, v41
	ds_bpermute_b32 v85, v70, v35
	ds_bpermute_b32 v87, v70, v45
	ds_bpermute_b32 v89, v70, v39
	ds_bpermute_b32 v91, v70, v47
	ds_bpermute_b32 v93, v70, v43
	ds_bpermute_b32 v80, v70, v32
	ds_bpermute_b32 v82, v70, v40
	ds_bpermute_b32 v84, v70, v34
	ds_bpermute_b32 v86, v70, v44
	ds_bpermute_b32 v88, v70, v38
	ds_bpermute_b32 v90, v70, v46
	ds_bpermute_b32 v92, v70, v42
	s_waitcnt lgkmcnt(14)
	v_pk_add_f32 v[78:79], v[36:37], v[78:79]
	s_waitcnt lgkmcnt(6)
	v_pk_add_f32 v[80:81], v[32:33], v[80:81]
	s_waitcnt lgkmcnt(5)
	v_pk_add_f32 v[82:83], v[40:41], v[82:83]
	s_waitcnt lgkmcnt(4)
	v_pk_add_f32 v[84:85], v[34:35], v[84:85]
	s_waitcnt lgkmcnt(3)
	v_pk_add_f32 v[86:87], v[44:45], v[86:87]
	s_waitcnt lgkmcnt(2)
	v_pk_add_f32 v[88:89], v[38:39], v[88:89]
	s_waitcnt lgkmcnt(1)
	v_pk_add_f32 v[90:91], v[46:47], v[90:91]
	s_waitcnt lgkmcnt(0)
	v_pk_add_f32 v[92:93], v[42:43], v[92:93]
	ds_bpermute_b32 v95, v71, v79
	ds_bpermute_b32 v94, v71, v78
	ds_bpermute_b32 v97, v71, v81
	ds_bpermute_b32 v96, v71, v80
	ds_bpermute_b32 v99, v71, v83
	ds_bpermute_b32 v98, v71, v82
	ds_bpermute_b32 v103, v71, v85
	ds_bpermute_b32 v102, v71, v84
	ds_bpermute_b32 v105, v71, v87
	ds_bpermute_b32 v104, v71, v86
	ds_bpermute_b32 v107, v71, v89
	ds_bpermute_b32 v106, v71, v88
	ds_bpermute_b32 v109, v71, v91
	ds_bpermute_b32 v108, v71, v90
	ds_bpermute_b32 v111, v71, v93
	ds_bpermute_b32 v110, v71, v92
	s_waitcnt lgkmcnt(14)
	v_pk_add_f32 v[78:79], v[78:79], v[94:95]
	s_waitcnt lgkmcnt(12)
	v_pk_add_f32 v[80:81], v[80:81], v[96:97]
	s_waitcnt lgkmcnt(10)
	v_pk_add_f32 v[82:83], v[82:83], v[98:99]
	s_waitcnt lgkmcnt(8)
	v_pk_add_f32 v[84:85], v[84:85], v[102:103]
	s_waitcnt lgkmcnt(6)
	v_pk_add_f32 v[86:87], v[86:87], v[104:105]
	s_waitcnt lgkmcnt(4)
	v_pk_add_f32 v[88:89], v[88:89], v[106:107]
	s_waitcnt lgkmcnt(2)
	v_pk_add_f32 v[90:91], v[90:91], v[108:109]
	s_waitcnt lgkmcnt(0)
	v_pk_add_f32 v[92:93], v[92:93], v[110:111]
	ds_bpermute_b32 v95, v72, v79
	ds_bpermute_b32 v94, v72, v78
	ds_bpermute_b32 v97, v72, v81
	ds_bpermute_b32 v96, v72, v80
	ds_bpermute_b32 v99, v72, v83
	ds_bpermute_b32 v98, v72, v82
	ds_bpermute_b32 v103, v72, v85
	ds_bpermute_b32 v102, v72, v84
	ds_bpermute_b32 v105, v72, v87
	ds_bpermute_b32 v104, v72, v86
	ds_bpermute_b32 v107, v72, v89
	ds_bpermute_b32 v106, v72, v88
	ds_bpermute_b32 v109, v72, v91
	ds_bpermute_b32 v108, v72, v90
	ds_bpermute_b32 v111, v72, v93
	ds_bpermute_b32 v110, v72, v92
	s_waitcnt lgkmcnt(14)
	v_pk_add_f32 v[78:79], v[78:79], v[94:95]
	s_waitcnt lgkmcnt(12)
	v_pk_add_f32 v[80:81], v[80:81], v[96:97]
	s_waitcnt lgkmcnt(10)
	v_pk_add_f32 v[82:83], v[82:83], v[98:99]
	s_waitcnt lgkmcnt(8)
	v_pk_add_f32 v[84:85], v[84:85], v[102:103]
	s_waitcnt lgkmcnt(6)
	v_pk_add_f32 v[86:87], v[86:87], v[104:105]
	s_waitcnt lgkmcnt(4)
	v_pk_add_f32 v[88:89], v[88:89], v[106:107]
	s_waitcnt lgkmcnt(2)
	v_pk_add_f32 v[90:91], v[90:91], v[108:109]
	s_waitcnt lgkmcnt(0)
	v_pk_add_f32 v[92:93], v[92:93], v[110:111]
	ds_bpermute_b32 v95, v73, v79
	ds_bpermute_b32 v94, v73, v78
	ds_bpermute_b32 v97, v73, v81
	ds_bpermute_b32 v96, v73, v80
	ds_bpermute_b32 v99, v73, v83
	ds_bpermute_b32 v98, v73, v82
	ds_bpermute_b32 v103, v73, v85
	ds_bpermute_b32 v102, v73, v84
	ds_bpermute_b32 v105, v73, v87
	ds_bpermute_b32 v104, v73, v86
	ds_bpermute_b32 v107, v73, v89
	ds_bpermute_b32 v106, v73, v88
	ds_bpermute_b32 v109, v73, v91
	ds_bpermute_b32 v108, v73, v90
	ds_bpermute_b32 v111, v73, v93
	ds_bpermute_b32 v110, v73, v92
	s_waitcnt lgkmcnt(14)
; __device__ __forceinline__ void phase_conv(Frame& F) {
;     ...
; #pragma unroll
;             for (int o = 1; o < 64; o <<= 1) {
;                 float ts[8], tq[8];
; #pragma unroll
;                 for (int q = 0; q < 8; ++q) { ts[q] = __shfl_xor(s[q], o); tq[q] = __shfl_xor(ss[q], o); }
; #pragma unroll
;                 for (int q = 0; q < 8; ++q) { s[q] += ts[q]; ss[q] += tq[q]; } }
	v_pk_add_f32 v[78:79], v[78:79], v[94:95]
	s_waitcnt lgkmcnt(12)
	v_pk_add_f32 v[80:81], v[80:81], v[96:97]
	s_waitcnt lgkmcnt(10)
	v_pk_add_f32 v[82:83], v[82:83], v[98:99]
	s_waitcnt lgkmcnt(8)
	v_pk_add_f32 v[84:85], v[84:85], v[102:103]
	s_waitcnt lgkmcnt(6)
	v_pk_add_f32 v[86:87], v[86:87], v[104:105]
	s_waitcnt lgkmcnt(4)
	v_pk_add_f32 v[88:89], v[88:89], v[106:107]
	s_waitcnt lgkmcnt(2)
	v_pk_add_f32 v[90:91], v[90:91], v[108:109]
	s_waitcnt lgkmcnt(0)
	v_pk_add_f32 v[92:93], v[92:93], v[110:111]
	ds_bpermute_b32 v95, v74, v79
	ds_bpermute_b32 v94, v74, v78
	ds_bpermute_b32 v97, v74, v81
	ds_bpermute_b32 v96, v74, v80
	ds_bpermute_b32 v99, v74, v83
	ds_bpermute_b32 v98, v74, v82
	ds_bpermute_b32 v103, v74, v85
	ds_bpermute_b32 v102, v74, v84
	ds_bpermute_b32 v105, v74, v87
	ds_bpermute_b32 v104, v74, v86
	ds_bpermute_b32 v107, v74, v89
	ds_bpermute_b32 v106, v74, v88
	ds_bpermute_b32 v109, v74, v91
	ds_bpermute_b32 v108, v74, v90
	ds_bpermute_b32 v111, v74, v93
	ds_bpermute_b32 v110, v74, v92
	s_waitcnt lgkmcnt(14)
	v_pk_add_f32 v[78:79], v[78:79], v[94:95]
	v_lshl_add_u64 v[4:5], v[2:3], 0, s[38:39]
	s_waitcnt lgkmcnt(12)
	v_pk_add_f32 v[80:81], v[80:81], v[96:97]
	s_waitcnt lgkmcnt(10)
	v_pk_add_f32 v[82:83], v[82:83], v[98:99]
	s_waitcnt lgkmcnt(8)
	v_pk_add_f32 v[84:85], v[84:85], v[102:103]
	s_waitcnt lgkmcnt(6)
	v_pk_add_f32 v[86:87], v[86:87], v[104:105]
	s_waitcnt lgkmcnt(4)
	v_pk_add_f32 v[88:89], v[88:89], v[106:107]
	s_waitcnt lgkmcnt(2)
	v_pk_add_f32 v[90:91], v[90:91], v[108:109]
	s_waitcnt lgkmcnt(0)
	v_pk_add_f32 v[92:93], v[92:93], v[110:111]
	ds_bpermute_b32 v95, v75, v79
	ds_bpermute_b32 v94, v75, v78
	v_add_co_u32_e32 v22, vcc, s9, v4
	ds_bpermute_b32 v97, v75, v81
	ds_bpermute_b32 v96, v75, v80
	ds_bpermute_b32 v99, v75, v83
	ds_bpermute_b32 v98, v75, v82
	ds_bpermute_b32 v103, v75, v85
	ds_bpermute_b32 v102, v75, v84
	ds_bpermute_b32 v105, v75, v87
	ds_bpermute_b32 v104, v75, v86
	ds_bpermute_b32 v107, v75, v89
	ds_bpermute_b32 v106, v75, v88
	ds_bpermute_b32 v109, v75, v91
	ds_bpermute_b32 v108, v75, v90
	ds_bpermute_b32 v111, v75, v93
	ds_bpermute_b32 v110, v75, v92
	v_addc_co_u32_e32 v23, vcc, 0, v5, vcc
	v_add_co_u32_e32 v24, vcc, s23, v4
	s_waitcnt lgkmcnt(14)
	v_pk_add_f32 v[78:79], v[78:79], v[94:95]
	v_addc_co_u32_e32 v25, vcc, 0, v5, vcc
	v_add_co_u32_e32 v26, vcc, s42, v4
	s_waitcnt lgkmcnt(12)
	v_pk_add_f32 v[80:81], v[80:81], v[96:97]
	v_addc_co_u32_e32 v27, vcc, 0, v5, vcc
	s_waitcnt lgkmcnt(10)
	v_pk_add_f32 v[82:83], v[82:83], v[98:99]
	s_waitcnt lgkmcnt(8)
	v_pk_add_f32 v[84:85], v[84:85], v[102:103]
	s_waitcnt lgkmcnt(6)
	v_pk_add_f32 v[86:87], v[86:87], v[104:105]
	s_waitcnt lgkmcnt(4)
	v_pk_add_f32 v[88:89], v[88:89], v[106:107]
	s_waitcnt lgkmcnt(2)
	v_pk_add_f32 v[90:91], v[90:91], v[108:109]
	s_waitcnt lgkmcnt(0)
; #define GAS __attribute__((address_space(1)))
; __device__ __forceinline__ unsigned f2bf(float f) { unsigned u = __builtin_bit_cast(unsigned, f); return (u + 0x7fffu + ((u >> 16) & 1u)) >> 16; }
; __device__ __forceinline__ void phase_conv(Frame& F) {
;     ...
;     for (int ti = F.vcu; ti < 544; ti += F.G) {
;         int rowbase, L, p0;
;         if (ti < 512) { rowbase = (ti >> 6) * SEQ; p0 = (ti & 63) * 64; L = SEQ; } else { const int q = ti - 512; rowbase = TL + (q >> 2) * CTXL; p0 = (q & 3) * 64; L = CTXL; }
;     ...
;             for (int q = 0; q < 8; ++q) { const float mean = s[q] * (1.f / 64.f), var = fmaxf(ss[q] * (1.f / 64.f) - mean * mean, 0.f);
;                 const float z = (a[q] - mean) * rsqrtf(var + EPSN) * lg + lb;
;                 ((GAS bf16*)MIX)[(size_t)(rowbase + p0 + ch * 8 + q) * 1536 + c] = (bf16)f2bf(z * __builtin_amdgcn_rcpf(1.f + __builtin_amdgcn_exp2f(-1.4426950408889634f * z))); }
	v_pk_add_f32 v[92:93], v[92:93], v[110:111]
	v_pk_mul_f32 v[78:79], v[78:79], s[22:23] op_sel_hi:[1,0]
	v_add_co_u32_e32 v28, vcc, s43, v4
	v_pk_mul_f32 v[80:81], v[80:81], s[22:23] op_sel_hi:[1,0]
	v_pk_mul_f32 v[82:83], v[82:83], s[22:23] op_sel_hi:[1,0]
	v_pk_mul_f32 v[84:85], v[84:85], s[22:23] op_sel_hi:[1,0]
	v_pk_mul_f32 v[86:87], v[86:87], s[22:23] op_sel_hi:[1,0]
	v_pk_mul_f32 v[88:89], v[88:89], s[22:23] op_sel_hi:[1,0]
	v_pk_mul_f32 v[90:91], v[90:91], s[22:23] op_sel_hi:[1,0]
	v_pk_mul_f32 v[92:93], v[92:93], s[22:23] op_sel_hi:[1,0]
	v_fma_f32 v32, -v79, v79, v78
	v_addc_co_u32_e32 v29, vcc, 0, v5, vcc
	v_sub_f32_e32 v34, v37, v79
	v_fma_f32 v36, -v81, v81, v80
	v_fma_f32 v37, -v83, v83, v82
	v_sub_f32_e32 v38, v41, v83
	v_fma_f32 v40, -v85, v85, v84
	v_fma_f32 v41, -v87, v87, v86
	v_sub_f32_e32 v42, v45, v87
	v_fma_f32 v44, -v89, v89, v88
	v_fma_f32 v45, -v91, v91, v90
	v_sub_f32_e32 v46, v47, v91
	v_fma_f32 v47, -v93, v93, v92
	v_max_f32_e32 v32, 0, v32
	v_add_u32_e32 v31, 0x2000, v100
	v_add_co_u32_e32 v30, vcc, 0x5000, v4
	v_max_f32_e32 v36, 0, v36
	v_max_f32_e32 v37, 0, v37
	v_max_f32_e32 v40, 0, v40
	v_max_f32_e32 v41, 0, v41
	v_max_f32_e32 v44, 0, v44
	v_max_f32_e32 v45, 0, v45
	v_max_f32_e32 v47, 0, v47
	v_add_f32_e32 v32, 0x358637bd, v32
	v_mov_b32_e32 v100, v31
	v_addc_co_u32_e32 v31, vcc, 0, v5, vcc
	v_add_f32_e32 v36, 0x358637bd, v36
	v_add_f32_e32 v37, 0x358637bd, v37
	v_add_f32_e32 v40, 0x358637bd, v40
	v_add_f32_e32 v41, 0x358637bd, v41
	v_add_f32_e32 v44, 0x358637bd, v44
	v_add_f32_e32 v45, 0x358637bd, v45
	v_add_f32_e32 v47, 0x358637bd, v47
	v_mul_f32_e32 v78, 0x4b800000, v32
	v_cmp_gt_f32_e64 s[16:17], s47, v32
	v_sub_f32_e32 v33, v33, v81
	v_sub_f32_e32 v35, v35, v85
	v_mul_f32_e32 v79, 0x4b800000, v36
	v_cmp_gt_f32_e32 vcc, s47, v36
	v_mul_f32_e32 v80, 0x4b800000, v37
	v_cmp_gt_f32_e64 s[0:1], s47, v37
	v_mul_f32_e32 v81, 0x4b800000, v40
	v_cmp_gt_f32_e64 s[2:3], s47, v40
	v_mul_f32_e32 v82, 0x4b800000, v41
	v_cmp_gt_f32_e64 s[4:5], s47, v41
	v_mul_f32_e32 v83, 0x4b800000, v44
	v_cmp_gt_f32_e64 s[10:11], s47, v44
	v_mul_f32_e32 v84, 0x4b800000, v45
	v_cmp_gt_f32_e64 s[12:13], s47, v45
	v_mul_f32_e32 v85, 0x4b800000, v47
	v_cmp_gt_f32_e64 s[14:15], s47, v47
	v_cndmask_b32_e64 v32, v32, v78, s[16:17]
	v_cndmask_b32_e32 v36, v36, v79, vcc
	v_cndmask_b32_e64 v37, v37, v80, s[0:1]
	v_cndmask_b32_e64 v40, v40, v81, s[2:3]
	v_cndmask_b32_e64 v41, v41, v82, s[4:5]
	v_cndmask_b32_e64 v44, v44, v83, s[10:11]
	v_cndmask_b32_e64 v45, v45, v84, s[12:13]
	v_cndmask_b32_e64 v47, v47, v85, s[14:15]
	v_rsq_f32_e32 v32, v32
	v_rsq_f32_e32 v36, v36
	v_rsq_f32_e32 v37, v37
	v_rsq_f32_e32 v40, v40
	v_rsq_f32_e32 v41, v41
	v_rsq_f32_e32 v44, v44
	v_rsq_f32_e32 v45, v45
	v_rsq_f32_e32 v47, v47
	v_mul_f32_e32 v78, 0x45800000, v32
	v_mul_f32_e32 v79, 0x45800000, v36
	v_mul_f32_e32 v80, 0x45800000, v37
	v_mul_f32_e32 v81, 0x45800000, v40
	v_mul_f32_e32 v82, 0x45800000, v41
	v_mul_f32_e32 v83, 0x45800000, v44
	v_mul_f32_e32 v84, 0x45800000, v45
	v_mul_f32_e32 v85, 0x45800000, v47
	v_cndmask_b32_e64 v32, v32, v78, s[16:17]
	v_sub_f32_e32 v39, v39, v89
	v_sub_f32_e32 v43, v43, v93
	v_cndmask_b32_e32 v36, v36, v79, vcc
	v_cndmask_b32_e64 v37, v37, v80, s[0:1]
	v_cndmask_b32_e64 v40, v40, v81, s[2:3]
	v_cndmask_b32_e64 v41, v41, v82, s[4:5]
	v_cndmask_b32_e64 v44, v44, v83, s[10:11]
	v_cndmask_b32_e64 v45, v45, v84, s[12:13]
	v_cndmask_b32_e64 v47, v47, v85, s[14:15]
	v_mul_f32_e32 v32, v34, v32
	v_mul_f32_e32 v33, v33, v36
	v_mul_f32_e32 v34, v38, v37
	v_mul_f32_e32 v35, v35, v40
	v_mul_f32_e32 v36, v42, v41
	v_mul_f32_e32 v37, v39, v44
	v_mul_f32_e32 v38, v46, v45
	v_mul_f32_e32 v39, v43, v47
	v_fma_f32 v32, v67, v32, v68
	v_fma_f32 v33, v67, v33, v68
	v_fma_f32 v34, v67, v34, v68
	v_fma_f32 v35, v67, v35, v68
	v_fma_f32 v36, v67, v36, v68
	v_fma_f32 v37, v67, v37, v68
	v_fma_f32 v38, v67, v38, v68
	v_fma_f32 v39, v67, v39, v68
	v_mul_f32_e32 v40, 0xbfb8aa3b, v32
	v_mul_f32_e32 v41, 0xbfb8aa3b, v33
	v_mul_f32_e32 v42, 0xbfb8aa3b, v34
	v_mul_f32_e32 v43, 0xbfb8aa3b, v35
	v_mul_f32_e32 v44, 0xbfb8aa3b, v36
	v_mul_f32_e32 v45, 0xbfb8aa3b, v37
	v_mul_f32_e32 v46, 0xbfb8aa3b, v38
	v_mul_f32_e32 v47, 0xbfb8aa3b, v39
	v_exp_f32_e32 v40, v40
	v_exp_f32_e32 v41, v41
	v_exp_f32_e32 v42, v42
	v_exp_f32_e32 v43, v43
	v_exp_f32_e32 v44, v44
	v_exp_f32_e32 v45, v45
	v_exp_f32_e32 v46, v46
	v_exp_f32_e32 v47, v47
	v_add_f32_e32 v40, 1.0, v40
	v_add_f32_e32 v41, 1.0, v41
	v_add_f32_e32 v42, 1.0, v42
	v_add_f32_e32 v43, 1.0, v43
	v_add_f32_e32 v44, 1.0, v44
	v_add_f32_e32 v45, 1.0, v45
	v_add_f32_e32 v46, 1.0, v46
	v_add_f32_e32 v47, 1.0, v47
	v_rcp_f32_e32 v40, v40
	v_rcp_f32_e32 v41, v41
	v_rcp_f32_e32 v42, v42
	v_rcp_f32_e32 v43, v43
	v_rcp_f32_e32 v44, v44
	v_rcp_f32_e32 v45, v45
	v_rcp_f32_e32 v46, v46
	v_rcp_f32_e32 v47, v47
	s_add_u32 s38, s38, 0x6000
	v_mul_f32_e32 v32, v32, v40
	s_addc_u32 s39, s39, 0
	v_mul_f32_e32 v33, v33, v41
	v_mul_f32_e32 v34, v34, v42
	v_mul_f32_e32 v35, v35, v43
	v_mul_f32_e32 v36, v36, v44
	v_mul_f32_e32 v37, v37, v45
	v_mul_f32_e32 v38, v38, v46
	v_mul_f32_e32 v39, v39, v47
	v_bfe_u32 v40, v32, 16, 1
	s_cmp_eq_u32 s38, s98
	v_bfe_u32 v41, v33, 16, 1
	v_bfe_u32 v42, v34, 16, 1
	v_bfe_u32 v43, v35, 16, 1
	v_bfe_u32 v44, v36, 16, 1
	v_bfe_u32 v45, v37, 16, 1
	v_bfe_u32 v46, v38, 16, 1
	v_bfe_u32 v47, v39, 16, 1
	v_add3_u32 v32, v32, v40, s48
	v_add3_u32 v33, v33, v41, s48
	v_add3_u32 v34, v34, v42, s48
	v_add3_u32 v35, v35, v43, s48
	v_add3_u32 v36, v36, v44, s48
	v_add3_u32 v37, v37, v45, s48
	v_add3_u32 v38, v38, v46, s48
	v_add3_u32 v39, v39, v47, s48
	global_store_short_d16_hi v[4:5], v32, off
	global_store_short_d16_hi v[4:5], v33, off offset:3072
	global_store_short_d16_hi v[22:23], v34, off offset:2048
	global_store_short_d16_hi v[24:25], v35, off offset:1024
	global_store_short_d16_hi v[26:27], v36, off
	global_store_short_d16_hi v[26:27], v37, off offset:3072
	global_store_short_d16_hi v[28:29], v38, off offset:2048
	global_store_short_d16_hi v[30:31], v39, off offset:1024
	s_cbranch_scc0 .LBB0_353
	s_cmp_lg_u32 s101, 0
	s_cbranch_scc1 .LBB0_355
	s_add_i32 s49, s49, s67
	s_cmpk_lg_i32 s67, 0x100
	s_cbranch_scc1 .Lconv_orig
	s_cmpk_lt_i32 s49, 0x200
	s_cbranch_scc1 .LBB0_345
	s_mov_b32 s101, 1
	s_lshr_b32 s49, s71, 3
	s_addk_i32 s49, 0x200
	s_and_b32 s100, s71, 7
	s_mul_i32 s99, s100, 0x6000
	s_lshl_b32 s100, s100, 13
	s_add_i32 s98, s99, 0x6000
	s_branch .LBB0_345
.Lconv_orig:
	s_cmpk_gt_i32 s49, 0x21f
	s_cbranch_scc0 .LBB0_345

; #define PG8_LAS __attribute__((address_space(3)))
; __device__ __forceinline__ u32x4 pack8(const f32x4& a, const f32x4& b) { u32x4 w; w.x = cvt_pk_bf16(a[0], a[1]); w.y = cvt_pk_bf16(a[2], a[3]); w.z = cvt_pk_bf16(b[0], b[1]); w.w = cvt_pk_bf16(b[2], b[3]); return w; }
;     __device__ __forceinline__ void st(const void* p, const u32x4& v) const { __builtin_amdgcn_raw_buffer_store_b128(v, r, (unsigned)((const unsigned char*)p - b), 0, EPI_SC1); }
;     __device__ __forceinline__ void operator()(const f32x4 (&acc)[2][2][4][2], const Unit& u, int wr, int wc, int fr, int fq) const { const WsStore W_(wsb);
;     ...
;         PG8_LAS unsigned char* stg = stg0 + (wr * 4 + wc) * 2048;
;         const int lane = fr + 16 * fq, rr = lane >> 3, ch = lane & 7;
;         const int row0 = u.pm * BM + wr * 64, col0 = coff + u.pn * BM + wc * 64 + ch * 8;
; #pragma unroll
;         for (int ai = 0; ai < 2; ++ai)
; #pragma unroll
;             for (int m = 0; m < 4; ++m) {
;                 if (EPI_DIRECT) {
; #pragma unroll
;                     for (int bj = 0; bj < 2; ++bj) W_.st(O + (size_t)(row0 + ai * HALF + m * 16 + fr) * ldc + coff + u.pn * BM + wc * 64 + bj * 32 + 8 * fq, pack8(acc[ai][bj][m][0], acc[ai][bj][m][1]));
;                     continue; }
; #pragma unroll
;                 for (int bj = 0; bj < 2; ++bj) *(PG8_LAS u32x4*)(stg + fr * 128 + (((bj * 4 + fq) ^ (fr & 7)) * 16)) = pack8(acc[ai][bj][m][0], acc[ai][bj][m][1]);
;                 asm volatile("s_waitcnt lgkmcnt(0)" ::: "memory");
;                 u32x4 w[2];
; #pragma unroll
;                 for (int r = 0; r < 2; ++r) { const int row = 8 * r + rr; w[r] = *(const PG8_LAS u32x4*)(stg + row * 128 + ((ch ^ (row & 7)) * 16)); }
;                 asm volatile("s_waitcnt lgkmcnt(0)" ::: "memory");
; #pragma unroll
;                 for (int r = 0; r < 2; ++r) W_.st(O + (size_t)(row0 + ai * HALF + m * 16 + 8 * r + rr) * ldc + col0, w[r]); }
.LBB0_510:
	v_mov_b32_e32 v144, v0
	v_cvt_pk_bf16_f32 v126, v126, v127
	v_cvt_pk_bf16_f32 v127, v128, v129
	v_cvt_pk_bf16_f32 v128, v118, v119
	v_cvt_pk_bf16_f32 v129, v120, v121
	s_lshl_b32 s23, s23, 8
	v_readfirstlane_b32 s14, v144
	s_ashr_i32 s15, s14, 8
	s_bfe_u32 s14, s14, 0x20006
	s_lshl_b32 s16, s15, 13
	s_lshl_b32 s30, s14, 11
	s_add_i32 s16, s16, 0
	s_add_i32 s16, s16, s30
	v_lshlrev_b32_e32 v151, 7, v144
	v_lshrrev_b32_e32 v145, 4, v144
	s_add_i32 s16, s16, 0x22000
	v_and_b32_e32 v149, 7, v144
	v_and_b32_e32 v151, 0x780, v151
	v_add_u32_e32 v151, s16, v151
	v_bitop3_b32 v118, v145, v149, 3 bitop3:0x6c
	v_bfe_u32 v146, v144, 4, 2
	v_lshl_add_u32 v145, v118, 4, v151
	v_lshrrev_b32_e32 v147, 3, v144
	ds_write_b128 v145, v[126:129]
	v_cvt_pk_bf16_f32 v118, v122, v123
	v_cvt_pk_bf16_f32 v119, v124, v125
	v_cvt_pk_bf16_f32 v120, v114, v115
	v_bitop3_b32 v114, v146, v149, 4 bitop3:0x36
	v_bfe_u32 v148, v144, 3, 3
	v_bitop3_b32 v144, v147, v144, 7 bitop3:0x28
	v_lshl_add_u32 v122, v114, 4, v151
	v_lshlrev_b32_e32 v152, 7, v148
	v_lshlrev_b32_e32 v144, 4, v144
	v_cvt_pk_bf16_f32 v121, v116, v117
	ds_write_b128 v122, v[118:121]
	v_add3_u32 v144, s16, v152, v144
	s_waitcnt lgkmcnt(0)
	s_lshl_b32 s15, s15, 6
	s_lshl_b32 s22, s22, 9
	ds_read_b128 v[114:117], v144
	ds_read_b128 v[118:121], v144 offset:1024
	s_add_i32 s15, s15, s23
	v_lshl_or_b32 v150, v149, 4, s22
	v_lshl_or_b32 v150, s14, 7, v150
	v_or_b32_e32 v147, s15, v148
	v_lshl_add_u32 v123, v147, 12, v150
	s_mov_b32 s22, s18
	s_mov_b32 s23, s19
	s_waitcnt lgkmcnt(0)
	s_waitcnt lgkmcnt(0)
	buffer_store_dwordx4 v[114:117], v123, s[20:23], 0 offen sc1
	s_andn2_b64 vcc, exec, s[2:3]
	s_mov_b64 s[2:3], -1
	v_add_u32_e32 v114, 0x8000, v123
	buffer_store_dwordx4 v[118:121], v114, s[20:23], 0 offen sc1
	v_cvt_pk_bf16_f32 v106, v106, v107
	v_cvt_pk_bf16_f32 v107, v108, v109
	v_cvt_pk_bf16_f32 v108, v98, v99
	v_cvt_pk_bf16_f32 v109, v100, v101
	ds_write_b128 v145, v[106:109]
	v_cvt_pk_bf16_f32 v98, v110, v111
	v_cvt_pk_bf16_f32 v99, v112, v113
	v_cvt_pk_bf16_f32 v100, v102, v103
	v_cvt_pk_bf16_f32 v101, v104, v105
	ds_write_b128 v122, v[98:101]
	s_waitcnt lgkmcnt(0)
	ds_read_b128 v[98:101], v144
	ds_read_b128 v[102:105], v144 offset:1024
	v_add_u32_e32 v106, 0x10000, v123
	s_waitcnt lgkmcnt(0)
	s_waitcnt lgkmcnt(0)
	buffer_store_dwordx4 v[98:101], v106, s[20:23], 0 offen sc1
	s_nop 1
	v_add_u32_e32 v98, 0x18000, v123
	buffer_store_dwordx4 v[102:105], v98, s[20:23], 0 offen sc1
	v_cvt_pk_bf16_f32 v90, v90, v91
	v_cvt_pk_bf16_f32 v91, v92, v93
	v_cvt_pk_bf16_f32 v92, v82, v83
	v_cvt_pk_bf16_f32 v93, v84, v85
	ds_write_b128 v145, v[90:93]
	v_cvt_pk_bf16_f32 v82, v94, v95
	v_cvt_pk_bf16_f32 v83, v96, v97
	v_cvt_pk_bf16_f32 v84, v86, v87
	v_cvt_pk_bf16_f32 v85, v88, v89
	ds_write_b128 v122, v[82:85]
	s_waitcnt lgkmcnt(0)
	ds_read_b128 v[82:85], v144
	ds_read_b128 v[86:89], v144 offset:1024
	v_add_u32_e32 v90, 0x20000, v123
	s_waitcnt lgkmcnt(0)
	s_waitcnt lgkmcnt(0)
	buffer_store_dwordx4 v[82:85], v90, s[20:23], 0 offen sc1
	s_nop 1
	v_add_u32_e32 v82, 0x28000, v123
	buffer_store_dwordx4 v[86:89], v82, s[20:23], 0 offen sc1
	v_cvt_pk_bf16_f32 v58, v58, v59
	v_cvt_pk_bf16_f32 v59, v60, v61
	v_cvt_pk_bf16_f32 v60, v50, v51
	v_cvt_pk_bf16_f32 v61, v52, v53
	ds_write_b128 v145, v[58:61]
	v_cvt_pk_bf16_f32 v50, v62, v63
	v_cvt_pk_bf16_f32 v51, v64, v65
	v_cvt_pk_bf16_f32 v52, v54, v55
	v_cvt_pk_bf16_f32 v53, v56, v57
	ds_write_b128 v122, v[50:53]
	s_waitcnt lgkmcnt(0)
	ds_read_b128 v[50:53], v144
	ds_read_b128 v[54:57], v144 offset:1024
	v_add_u32_e32 v58, 0x30000, v123
	s_waitcnt lgkmcnt(0)
	s_waitcnt lgkmcnt(0)
	buffer_store_dwordx4 v[50:53], v58, s[20:23], 0 offen sc1
	v_add_u32_e32 v58, 0x80000, v123
	s_nop 0
	v_add_u32_e32 v50, 0x38000, v123
	buffer_store_dwordx4 v[54:57], v50, s[20:23], 0 offen sc1
	v_cvt_pk_bf16_f32 v50, v74, v75
	v_cvt_pk_bf16_f32 v51, v76, v77
	v_cvt_pk_bf16_f32 v52, v66, v67
	v_cvt_pk_bf16_f32 v53, v68, v69
	ds_write_b128 v145, v[50:53]
	v_cvt_pk_bf16_f32 v50, v78, v79
	v_cvt_pk_bf16_f32 v51, v80, v81
	v_cvt_pk_bf16_f32 v52, v70, v71
	v_cvt_pk_bf16_f32 v53, v72, v73
	ds_write_b128 v122, v[50:53]
	s_waitcnt lgkmcnt(0)
	ds_read_b128 v[50:53], v144
	ds_read_b128 v[54:57], v144 offset:1024
	s_waitcnt lgkmcnt(0)
	s_waitcnt lgkmcnt(0)
	buffer_store_dwordx4 v[50:53], v58, s[20:23], 0 offen sc1
	s_nop 1
	v_add_u32_e32 v50, 0x88000, v123
	buffer_store_dwordx4 v[54:57], v50, s[20:23], 0 offen sc1
	v_cvt_pk_bf16_f32 v42, v42, v43
	v_cvt_pk_bf16_f32 v43, v44, v45
	v_cvt_pk_bf16_f32 v44, v34, v35
	v_cvt_pk_bf16_f32 v45, v36, v37
	ds_write_b128 v145, v[42:45]
	v_cvt_pk_bf16_f32 v34, v46, v47
	v_cvt_pk_bf16_f32 v35, v48, v49
	v_cvt_pk_bf16_f32 v36, v38, v39
	v_cvt_pk_bf16_f32 v37, v40, v41
	ds_write_b128 v122, v[34:37]
	s_waitcnt lgkmcnt(0)
	ds_read_b128 v[34:37], v144
	ds_read_b128 v[38:41], v144 offset:1024
	v_add_u32_e32 v42, 0x90000, v123
	s_waitcnt lgkmcnt(0)
	s_waitcnt lgkmcnt(0)
	buffer_store_dwordx4 v[34:37], v42, s[20:23], 0 offen sc1
	s_nop 1
	v_add_u32_e32 v34, 0x98000, v123
	buffer_store_dwordx4 v[38:41], v34, s[20:23], 0 offen sc1
	v_cvt_pk_bf16_f32 v26, v26, v27
	v_cvt_pk_bf16_f32 v27, v28, v29
	v_cvt_pk_bf16_f32 v28, v18, v19
	v_cvt_pk_bf16_f32 v29, v20, v21
	ds_write_b128 v145, v[26:29]
	v_cvt_pk_bf16_f32 v18, v30, v31
	v_cvt_pk_bf16_f32 v19, v32, v33
	v_cvt_pk_bf16_f32 v20, v22, v23
	v_cvt_pk_bf16_f32 v21, v24, v25
	ds_write_b128 v122, v[18:21]
	s_waitcnt lgkmcnt(0)
	ds_read_b128 v[18:21], v144
	ds_read_b128 v[22:25], v144 offset:1024
	v_add_u32_e32 v26, 0xa0000, v123
	s_waitcnt lgkmcnt(0)
	s_waitcnt lgkmcnt(0)
	buffer_store_dwordx4 v[18:21], v26, s[20:23], 0 offen sc1
	s_nop 1
	v_add_u32_e32 v18, 0xa8000, v123
	buffer_store_dwordx4 v[22:25], v18, s[20:23], 0 offen sc1
	v_cvt_pk_bf16_f32 v10, v10, v11
	v_cvt_pk_bf16_f32 v11, v12, v13
	v_cvt_pk_bf16_f32 v12, v2, v3
	v_cvt_pk_bf16_f32 v13, v4, v5
	ds_write_b128 v145, v[10:13]
	v_cvt_pk_bf16_f32 v2, v14, v15
	v_cvt_pk_bf16_f32 v3, v16, v17
	v_cvt_pk_bf16_f32 v4, v6, v7
	v_cvt_pk_bf16_f32 v5, v8, v9
	ds_write_b128 v122, v[2:5]
	s_waitcnt lgkmcnt(0)
	ds_read_b128 v[2:5], v144
	ds_read_b128 v[6:9], v144 offset:1024
	s_waitcnt lgkmcnt(0)
	v_add_u32_e32 v10, 0xb0000, v123
	s_waitcnt lgkmcnt(0)
	buffer_store_dwordx4 v[2:5], v10, s[20:23], 0 offen sc1
	s_nop 1
	v_add_u32_e32 v2, 0xb8000, v123
	buffer_store_dwordx4 v[6:9], v2, s[20:23], 0 offen sc1
	s_cbranch_vccnz .LBB0_499
	s_andn2_b64 vcc, exec, s[4:5]
	s_cbranch_vccnz .LBB0_498
	s_barrier
	s_branch .LBB0_498

; #define PG8_LAS __attribute__((address_space(3)))
; __device__ __forceinline__ u32x4 pack8(const f32x4& a, const f32x4& b) { u32x4 w; w.x = cvt_pk_bf16(a[0], a[1]); w.y = cvt_pk_bf16(a[2], a[3]); w.z = cvt_pk_bf16(b[0], b[1]); w.w = cvt_pk_bf16(b[2], b[3]); return w; }
;     __device__ __forceinline__ void st(const void* p, const u32x4& v) const { __builtin_amdgcn_raw_buffer_store_b128(v, r, (unsigned)((const unsigned char*)p - b), 0, EPI_SC1); }
;     __device__ __forceinline__ void operator()(const f32x4 (&acc)[2][2][4][2], const Unit& u, int wr, int wc, int fr, int fq) const { const WsStore W_(wsb);
;     ...
;         PG8_LAS unsigned char* stg = stg0 + (wr * 4 + wc) * 2048;
;         const int lane = fr + 16 * fq, rr = lane >> 3, ch = lane & 7;
;         const int row0 = u.pm * BM + wr * 64, col0 = coff + u.pn * BM + wc * 64 + ch * 8;
; #pragma unroll
;         for (int ai = 0; ai < 2; ++ai)
; #pragma unroll
;             for (int m = 0; m < 4; ++m) {
;                 if (EPI_DIRECT) {
; #pragma unroll
;                     for (int bj = 0; bj < 2; ++bj) W_.st(O + (size_t)(row0 + ai * HALF + m * 16 + fr) * ldc + coff + u.pn * BM + wc * 64 + bj * 32 + 8 * fq, pack8(acc[ai][bj][m][0], acc[ai][bj][m][1]));
;                     continue; }
; #pragma unroll
;                 for (int bj = 0; bj < 2; ++bj) *(PG8_LAS u32x4*)(stg + fr * 128 + (((bj * 4 + fq) ^ (fr & 7)) * 16)) = pack8(acc[ai][bj][m][0], acc[ai][bj][m][1]);
;                 asm volatile("s_waitcnt lgkmcnt(0)" ::: "memory");
;                 u32x4 w[2];
; #pragma unroll
;                 for (int r = 0; r < 2; ++r) { const int row = 8 * r + rr; w[r] = *(const PG8_LAS u32x4*)(stg + row * 128 + ((ch ^ (row & 7)) * 16)); }
;                 asm volatile("s_waitcnt lgkmcnt(0)" ::: "memory");
; #pragma unroll
;                 for (int r = 0; r < 2; ++r) W_.st(O + (size_t)(row0 + ai * HALF + m * 16 + 8 * r + rr) * ldc + col0, w[r]); }
.LBB0_524:
	v_mov_b32_e32 v140, v0
	v_cvt_pk_bf16_f32 v126, v126, v127
	v_cvt_pk_bf16_f32 v127, v128, v129
	v_cvt_pk_bf16_f32 v128, v118, v119
	v_cvt_pk_bf16_f32 v129, v120, v121
	s_lshl_b32 s53, s53, 8
	v_readfirstlane_b32 s30, v140
	s_ashr_i32 s31, s30, 8
	s_bfe_u32 s30, s30, 0x20006
	s_lshl_b32 s54, s31, 13
	s_lshl_b32 s55, s30, 11
	s_add_i32 s54, s54, 0
	s_add_i32 s54, s54, s55
	v_lshlrev_b32_e32 v147, 7, v140
	v_lshrrev_b32_e32 v141, 4, v140
	s_add_i32 s54, s54, 0x22000
	v_and_b32_e32 v145, 7, v140
	v_and_b32_e32 v147, 0x780, v147
	v_add_u32_e32 v147, s54, v147
	v_bitop3_b32 v118, v141, v145, 3 bitop3:0x6c
	v_bfe_u32 v142, v140, 4, 2
	v_lshl_add_u32 v141, v118, 4, v147
	v_lshrrev_b32_e32 v143, 3, v140
	ds_write_b128 v141, v[126:129]
	v_cvt_pk_bf16_f32 v118, v122, v123
	v_cvt_pk_bf16_f32 v119, v124, v125
	v_cvt_pk_bf16_f32 v120, v114, v115
	v_bitop3_b32 v114, v142, v145, 4 bitop3:0x36
	v_bfe_u32 v144, v140, 3, 3
	v_bitop3_b32 v140, v143, v140, 7 bitop3:0x28
	v_lshl_add_u32 v122, v114, 4, v147
	v_lshlrev_b32_e32 v148, 7, v144
	v_lshlrev_b32_e32 v140, 4, v140
	v_cvt_pk_bf16_f32 v121, v116, v117
	ds_write_b128 v122, v[118:121]
	s_lshl_b32 s31, s31, 6
	s_lshl_b32 s52, s52, 9
	v_add3_u32 v140, s54, v148, v140
	s_waitcnt lgkmcnt(0)
	s_add_i32 s31, s31, s53
	v_lshl_or_b32 v146, v145, 4, s52
	ds_read_b128 v[114:117], v140
	ds_read_b128 v[118:121], v140 offset:1024
	v_lshl_or_b32 v146, s30, 7, v146
	v_or_b32_e32 v143, s31, v144
	v_lshl_add_u32 v123, v143, 11, v146
	v_add_u32_e32 v124, 0x19a00000, v123
	s_waitcnt lgkmcnt(0)
	s_waitcnt lgkmcnt(0)
	buffer_store_dwordx4 v[114:117], v124, s[12:15], 0 offen sc1
	s_andn2_b64 vcc, exec, s[10:11]
	s_mov_b64 s[10:11], -1
	v_add_u32_e32 v114, 0x19a04000, v123
	buffer_store_dwordx4 v[118:121], v114, s[12:15], 0 offen sc1
	v_cvt_pk_bf16_f32 v106, v106, v107
	v_cvt_pk_bf16_f32 v107, v108, v109
	v_cvt_pk_bf16_f32 v108, v98, v99
	v_cvt_pk_bf16_f32 v109, v100, v101
	ds_write_b128 v141, v[106:109]
	v_cvt_pk_bf16_f32 v98, v110, v111
	v_cvt_pk_bf16_f32 v99, v112, v113
	v_cvt_pk_bf16_f32 v100, v102, v103
	v_cvt_pk_bf16_f32 v101, v104, v105
	ds_write_b128 v122, v[98:101]
	s_waitcnt lgkmcnt(0)
	ds_read_b128 v[98:101], v140
	ds_read_b128 v[102:105], v140 offset:1024
	v_add_u32_e32 v106, 0x19a08000, v123
	s_waitcnt lgkmcnt(0)
	s_waitcnt lgkmcnt(0)
	buffer_store_dwordx4 v[98:101], v106, s[12:15], 0 offen sc1
	s_nop 1
	v_add_u32_e32 v98, 0x19a0c000, v123
	buffer_store_dwordx4 v[102:105], v98, s[12:15], 0 offen sc1
	v_cvt_pk_bf16_f32 v90, v90, v91
	v_cvt_pk_bf16_f32 v91, v92, v93
	v_cvt_pk_bf16_f32 v92, v82, v83
	v_cvt_pk_bf16_f32 v93, v84, v85
	ds_write_b128 v141, v[90:93]
	v_cvt_pk_bf16_f32 v82, v94, v95
	v_cvt_pk_bf16_f32 v83, v96, v97
	v_cvt_pk_bf16_f32 v84, v86, v87
	v_cvt_pk_bf16_f32 v85, v88, v89
	ds_write_b128 v122, v[82:85]
	s_waitcnt lgkmcnt(0)
	ds_read_b128 v[82:85], v140
	ds_read_b128 v[86:89], v140 offset:1024
	v_add_u32_e32 v90, 0x19a10000, v123
	s_waitcnt lgkmcnt(0)
	s_waitcnt lgkmcnt(0)
	buffer_store_dwordx4 v[82:85], v90, s[12:15], 0 offen sc1
	s_nop 1
	v_add_u32_e32 v82, 0x19a14000, v123
	buffer_store_dwordx4 v[86:89], v82, s[12:15], 0 offen sc1
	v_cvt_pk_bf16_f32 v58, v58, v59
	v_cvt_pk_bf16_f32 v59, v60, v61
	v_cvt_pk_bf16_f32 v60, v50, v51
	v_cvt_pk_bf16_f32 v61, v52, v53
	ds_write_b128 v141, v[58:61]
	v_cvt_pk_bf16_f32 v50, v62, v63
	v_cvt_pk_bf16_f32 v51, v64, v65
	v_cvt_pk_bf16_f32 v52, v54, v55
	v_cvt_pk_bf16_f32 v53, v56, v57
	ds_write_b128 v122, v[50:53]
	s_waitcnt lgkmcnt(0)
	ds_read_b128 v[50:53], v140
	ds_read_b128 v[54:57], v140 offset:1024
	v_add_u32_e32 v58, 0x19a18000, v123
	s_waitcnt lgkmcnt(0)
	s_waitcnt lgkmcnt(0)
	buffer_store_dwordx4 v[50:53], v58, s[12:15], 0 offen sc1
	v_add_u32_e32 v58, 0x19a40000, v123
	s_nop 0
	v_add_u32_e32 v50, 0x19a1c000, v123
	buffer_store_dwordx4 v[54:57], v50, s[12:15], 0 offen sc1
	v_cvt_pk_bf16_f32 v50, v74, v75
	v_cvt_pk_bf16_f32 v51, v76, v77
	v_cvt_pk_bf16_f32 v52, v66, v67
	v_cvt_pk_bf16_f32 v53, v68, v69
	ds_write_b128 v141, v[50:53]
	v_cvt_pk_bf16_f32 v50, v78, v79
	v_cvt_pk_bf16_f32 v51, v80, v81
	v_cvt_pk_bf16_f32 v52, v70, v71
	v_cvt_pk_bf16_f32 v53, v72, v73
	ds_write_b128 v122, v[50:53]
	s_waitcnt lgkmcnt(0)
	ds_read_b128 v[50:53], v140
	ds_read_b128 v[54:57], v140 offset:1024
	s_waitcnt lgkmcnt(0)
	s_waitcnt lgkmcnt(0)
	buffer_store_dwordx4 v[50:53], v58, s[12:15], 0 offen sc1
	s_nop 1
	v_add_u32_e32 v50, 0x19a44000, v123
	buffer_store_dwordx4 v[54:57], v50, s[12:15], 0 offen sc1
	v_cvt_pk_bf16_f32 v42, v42, v43
	v_cvt_pk_bf16_f32 v43, v44, v45
	v_cvt_pk_bf16_f32 v44, v34, v35
	v_cvt_pk_bf16_f32 v45, v36, v37
	ds_write_b128 v141, v[42:45]
	v_cvt_pk_bf16_f32 v34, v46, v47
	v_cvt_pk_bf16_f32 v35, v48, v49
	v_cvt_pk_bf16_f32 v36, v38, v39
	v_cvt_pk_bf16_f32 v37, v40, v41
	ds_write_b128 v122, v[34:37]
	s_waitcnt lgkmcnt(0)
	ds_read_b128 v[34:37], v140
	ds_read_b128 v[38:41], v140 offset:1024
	v_add_u32_e32 v42, 0x19a48000, v123
	s_waitcnt lgkmcnt(0)
	s_waitcnt lgkmcnt(0)
	buffer_store_dwordx4 v[34:37], v42, s[12:15], 0 offen sc1
	s_nop 1
	v_add_u32_e32 v34, 0x19a4c000, v123
	buffer_store_dwordx4 v[38:41], v34, s[12:15], 0 offen sc1
	v_cvt_pk_bf16_f32 v26, v26, v27
	v_cvt_pk_bf16_f32 v27, v28, v29
	v_cvt_pk_bf16_f32 v28, v18, v19
	v_cvt_pk_bf16_f32 v29, v20, v21
	ds_write_b128 v141, v[26:29]
	v_cvt_pk_bf16_f32 v18, v30, v31
	v_cvt_pk_bf16_f32 v19, v32, v33
	v_cvt_pk_bf16_f32 v20, v22, v23
	v_cvt_pk_bf16_f32 v21, v24, v25
	ds_write_b128 v122, v[18:21]
	s_waitcnt lgkmcnt(0)
	ds_read_b128 v[18:21], v140
	ds_read_b128 v[22:25], v140 offset:1024
	v_add_u32_e32 v26, 0x19a50000, v123
	s_waitcnt lgkmcnt(0)
	s_waitcnt lgkmcnt(0)
	buffer_store_dwordx4 v[18:21], v26, s[12:15], 0 offen sc1
	s_nop 1
	v_add_u32_e32 v18, 0x19a54000, v123
	buffer_store_dwordx4 v[22:25], v18, s[12:15], 0 offen sc1
	v_cvt_pk_bf16_f32 v10, v10, v11
	v_cvt_pk_bf16_f32 v11, v12, v13
	v_cvt_pk_bf16_f32 v12, v2, v3
	v_cvt_pk_bf16_f32 v13, v4, v5
	ds_write_b128 v141, v[10:13]
	v_cvt_pk_bf16_f32 v2, v14, v15
	v_cvt_pk_bf16_f32 v3, v16, v17
	v_cvt_pk_bf16_f32 v4, v6, v7
	v_cvt_pk_bf16_f32 v5, v8, v9
	ds_write_b128 v122, v[2:5]
	s_waitcnt lgkmcnt(0)
	ds_read_b128 v[2:5], v140
	ds_read_b128 v[6:9], v140 offset:1024
	s_waitcnt lgkmcnt(0)
	v_add_u32_e32 v10, 0x19a58000, v123
	s_waitcnt lgkmcnt(0)
	buffer_store_dwordx4 v[2:5], v10, s[12:15], 0 offen sc1
	s_nop 1
	v_add_u32_e32 v2, 0x19a5c000, v123
	buffer_store_dwordx4 v[6:9], v2, s[12:15], 0 offen sc1
	s_cbranch_vccnz .LBB0_519
	s_andn2_b64 vcc, exec, s[4:5]
	s_cbranch_vccnz .LBB0_518
	s_barrier
	s_branch .LBB0_518

; #define PG8_LAS __attribute__((address_space(3)))
;     __device__ __forceinline__ void st(const void* p, const u32x4& v) const { __builtin_amdgcn_raw_buffer_store_b128(v, r, (unsigned)((const unsigned char*)p - b), 0, EPI_SC1); }
;     __device__ __forceinline__ void operator()(const f32x4 (&acc)[2][2][4][2], const Unit& u, int wr, int wc, int fr, int fq) const { const WsStore W_(wsb);
;     ...
;         PG8_LAS unsigned char* stg = stg0 + (wr * 4 + wc) * 2048;
;         const int lane = fr + 16 * fq, rr = lane >> 2, ch = lane & 3;
;         const size_t row0 = (size_t)u.pm * BM + wr * 64; const int col0 = u.pn * BM + wc * 64 + ch * 16;
;         float cl_hi = 432.f; asm volatile("" : "+v"(cl_hi));
; #pragma unroll
;         for (int ai = 0; ai < 2; ++ai)
; #pragma unroll
;             for (int m = 0; m < 4; ++m) {
; #pragma unroll
;                 for (int bj = 0; bj < 2; ++bj) { u32x2 w; f32x4 v0 = acc[ai][bj][m][0], v1 = acc[ai][bj][m][1];
; #pragma unroll
;                     for (int j = 0; j < 4; ++j) { asm("v_med3_f32 %0, %1, %2, %3" : "=v"(v0[j]) : "v"(v0[j]), "s"(-432.f), "v"(cl_hi)); asm("v_med3_f32 %0, %1, %2, %3" : "=v"(v1[j]) : "v"(v1[j]), "s"(-432.f), "v"(cl_hi)); }
;                     int p = 0; p = __builtin_amdgcn_cvt_pk_fp8_f32(v0[0], v0[1], p, false); p = __builtin_amdgcn_cvt_pk_fp8_f32(v0[2], v0[3], p, true); w.x = (unsigned)p;
;                     p = 0; p = __builtin_amdgcn_cvt_pk_fp8_f32(v1[0], v1[1], p, false); p = __builtin_amdgcn_cvt_pk_fp8_f32(v1[2], v1[3], p, true); w.y = (unsigned)p;
;                     *(PG8_LAS u32x2*)(stg + fr * 64 + (((bj * 4 + fq) ^ ((fr & 3) << 1)) * 8)) = w; }
;                 asm volatile("s_waitcnt lgkmcnt(0)" ::: "memory");
;                 const u32x4 w4 = *(const PG8_LAS u32x4*)(stg + rr * 64 + (((2 * ch) ^ ((rr & 3) << 1)) * 8));
;                 asm volatile("s_waitcnt lgkmcnt(0)" ::: "memory");
;                 if (FP8_ST_NT) W_.st_nt(O8 + (row0 + ai * HALF + m * 16 + rr) * 1024 + col0, w4); else W_.st(O8 + (row0 + ai * HALF + m * 16 + rr) * 1024 + col0, w4); }
.LBB0_879:
	v_mov_b32_e32 v140, v0
	s_lshl_b32 s58, s58, 8
	v_readfirstlane_b32 s30, v140
	s_ashr_i32 s31, s30, 8
	s_bfe_u32 s30, s30, 0x20006
	s_lshl_b32 s60, s31, 13
	s_lshl_b32 s31, s31, 6
	s_lshl_b32 s61, s30, 11
	s_add_i32 s31, s31, s58
	s_lshl_b32 s58, s59, 8
	s_lshl_b32 s30, s30, 6
	s_or_b32 s30, s30, s58
	v_lshlrev_b32_e32 v141, 4, v140
	v_lshrrev_b32_e32 v144, 2, v140
	v_bfe_u32 v145, v140, 2, 4
	v_and_or_b32 v146, v141, 48, s30
	v_mov_b32_e32 v141, 0x43d80000
	v_and_b32_e32 v142, 15, v140
	v_bfe_u32 v143, v140, 4, 2
	v_lshlrev_b32_e32 v147, 1, v140
	v_lshlrev_b32_e32 v149, 6, v145
	v_xor_b32_e32 v140, v144, v140
	v_or_b32_e32 v144, s31, v145
	v_med3_f32 v145, v122, s55, v141
	v_mov_b32_e32 v122, 0
	v_med3_f32 v123, v123, s55, v141
	v_med3_f32 v125, v125, s55, v141
	v_med3_f32 v124, v124, s55, v141
	v_med3_f32 v115, v115, s55, v141
	v_med3_f32 v118, v118, s55, v141
	v_med3_f32 v119, v119, s55, v141
	s_nop 0
	v_cvt_pk_fp8_f32 v122, v145, v123
	v_med3_f32 v120, v120, s55, v141
	v_med3_f32 v107, v107, s55, v141
	v_med3_f32 v108, v108, s55, v141
	v_cvt_pk_fp8_f32 v122, v124, v125 op_sel:[0,0,1]
	v_med3_f32 v125, v114, s55, v141
	v_mov_b32_e32 v114, 0
	v_cvt_pk_fp8_f32 v114, v125, v115
	v_mov_b32_e32 v115, 0
	v_cvt_pk_fp8_f32 v115, v118, v119
	v_med3_f32 v118, v121, s55, v141
	v_med3_f32 v109, v109, s55, v141
	v_med3_f32 v99, v99, s55, v141
	v_med3_f32 v102, v102, s55, v141
	v_med3_f32 v103, v103, s55, v141
	v_med3_f32 v104, v104, s55, v141
	s_nop 0
	v_cvt_pk_fp8_f32 v115, v120, v118 op_sel:[0,0,1]
	v_med3_f32 v120, v106, s55, v141
	v_mov_b32_e32 v106, 0
	v_cvt_pk_fp8_f32 v106, v120, v107
	v_med3_f32 v91, v91, s55, v141
	v_med3_f32 v92, v92, s55, v141
	v_med3_f32 v93, v93, s55, v141
	v_cvt_pk_fp8_f32 v106, v108, v109 op_sel:[0,0,1]
	v_med3_f32 v108, v98, s55, v141
	v_mov_b32_e32 v98, 0
	v_cvt_pk_fp8_f32 v98, v108, v99
	v_mov_b32_e32 v99, 0
	v_cvt_pk_fp8_f32 v99, v102, v103
	v_med3_f32 v102, v105, s55, v141
	v_med3_f32 v83, v83, s55, v141
	v_med3_f32 v86, v86, s55, v141
	v_med3_f32 v87, v87, s55, v141
	v_mov_b32_e32 v123, 0
	v_cvt_pk_fp8_f32 v99, v104, v102 op_sel:[0,0,1]
	v_med3_f32 v102, v90, s55, v141
	v_mov_b32_e32 v90, 0
	v_cvt_pk_fp8_f32 v90, v102, v91
	v_med3_f32 v88, v88, s55, v141
	v_med3_f32 v126, v126, s55, v141
	v_med3_f32 v127, v127, s55, v141
	v_cvt_pk_fp8_f32 v90, v92, v93 op_sel:[0,0,1]
	v_med3_f32 v92, v82, s55, v141
	v_mov_b32_e32 v82, 0
	v_cvt_pk_fp8_f32 v82, v92, v83
	v_mov_b32_e32 v83, 0
	v_cvt_pk_fp8_f32 v83, v86, v87
	v_med3_f32 v86, v89, s55, v141
	v_cvt_pk_fp8_f32 v123, v126, v127
	v_med3_f32 v75, v75, s55, v141
	v_cvt_pk_fp8_f32 v83, v88, v86 op_sel:[0,0,1]
	v_med3_f32 v86, v74, s55, v141
	v_mov_b32_e32 v74, 0
	v_cvt_pk_fp8_f32 v74, v86, v75
	s_add_i32 s60, s60, 0
	v_med3_f32 v76, v76, s55, v141
	s_add_i32 s60, s60, s61
	v_med3_f32 v128, v128, s55, v141
	v_med3_f32 v126, v129, s55, v141
	v_med3_f32 v116, v116, s55, v141
	v_med3_f32 v117, v117, s55, v141
	v_med3_f32 v77, v77, s55, v141
	v_med3_f32 v67, v67, s55, v141
	s_add_i32 s60, s60, 0x22000
	v_cvt_pk_fp8_f32 v123, v128, v126 op_sel:[0,0,1]
	v_cvt_pk_fp8_f32 v114, v116, v117 op_sel:[0,0,1]
	v_cvt_pk_fp8_f32 v74, v76, v77 op_sel:[0,0,1]
	v_med3_f32 v76, v66, s55, v141
	v_mov_b32_e32 v66, 0
	v_and_b32_e32 v148, 6, v147
	v_cvt_pk_fp8_f32 v66, v76, v67
	v_mov_b32_e32 v67, 0
	v_lshl_add_u32 v142, v142, 6, s60
	v_bitop3_b32 v124, v147, v143, 6 bitop3:0x6c
	v_bitop3_b32 v116, v143, v148, 4 bitop3:0x36
	v_mov_b32_e32 v107, 0
	v_med3_f32 v70, v70, s55, v141
	v_med3_f32 v71, v71, s55, v141
	v_lshlrev_b32_e32 v140, 4, v140
	v_cvt_pk_fp8_f32 v67, v70, v71
	v_lshl_add_u32 v124, v124, 3, v142
	v_lshl_add_u32 v118, v116, 3, v142
	v_med3_f32 v110, v110, s55, v141
	v_med3_f32 v111, v111, s55, v141
	v_and_b32_e32 v140, 48, v140
	v_cvt_pk_fp8_f32 v107, v110, v111
	ds_write_b64 v124, v[122:123]
	ds_write_b64 v118, v[114:115]
	v_add3_u32 v140, s60, v149, v140
	s_waitcnt lgkmcnt(0)
	v_med3_f32 v70, v73, s55, v141
	ds_read_b128 v[114:117], v140
	v_med3_f32 v72, v72, s55, v141
	v_med3_f32 v112, v112, s55, v141
	v_med3_f32 v110, v113, s55, v141
	v_med3_f32 v59, v59, s55, v141
	v_med3_f32 v100, v100, s55, v141
	v_med3_f32 v101, v101, s55, v141
	s_nop 0
	v_cvt_pk_fp8_f32 v67, v72, v70 op_sel:[0,0,1]
	v_med3_f32 v70, v58, s55, v141
	v_mov_b32_e32 v58, 0
	v_cvt_pk_fp8_f32 v107, v112, v110 op_sel:[0,0,1]
	v_cvt_pk_fp8_f32 v58, v70, v59
	v_cvt_pk_fp8_f32 v98, v100, v101 op_sel:[0,0,1]
	v_lshl_add_u32 v119, v144, 10, v146
	v_mov_b32_e32 v91, 0
	v_add_u32_e32 v100, 0x14c00000, v119
	v_med3_f32 v94, v94, s55, v141
	v_med3_f32 v95, v95, s55, v141
	v_med3_f32 v60, v60, s55, v141
	s_waitcnt lgkmcnt(0)
	s_waitcnt lgkmcnt(0)
	buffer_store_dwordx4 v[114:117], v100, s[12:15], 0 offen nt sc1
	v_cvt_pk_fp8_f32 v91, v94, v95
	ds_write_b64 v124, v[106:107]
	ds_write_b64 v118, v[98:99]
	v_med3_f32 v61, v61, s55, v141
	v_med3_f32 v51, v51, s55, v141
	s_waitcnt lgkmcnt(0)
	ds_read_b128 v[98:101], v140
	v_cvt_pk_fp8_f32 v58, v60, v61 op_sel:[0,0,1]
	v_med3_f32 v60, v50, s55, v141
	v_mov_b32_e32 v50, 0
	v_cvt_pk_fp8_f32 v50, v60, v51
	v_mov_b32_e32 v51, 0
	v_med3_f32 v54, v54, s55, v141
	v_med3_f32 v55, v55, s55, v141
	v_med3_f32 v96, v96, s55, v141
	v_med3_f32 v94, v97, s55, v141
	v_med3_f32 v84, v84, s55, v141
	v_med3_f32 v85, v85, s55, v141
	v_mov_b32_e32 v75, 0
	v_cvt_pk_fp8_f32 v51, v54, v55
	v_cvt_pk_fp8_f32 v91, v96, v94 op_sel:[0,0,1]
	v_cvt_pk_fp8_f32 v82, v84, v85 op_sel:[0,0,1]
	v_med3_f32 v54, v57, s55, v141
	v_add_u32_e32 v84, 0x14c04000, v119
	v_med3_f32 v78, v78, s55, v141
	v_med3_f32 v79, v79, s55, v141
	v_med3_f32 v56, v56, s55, v141
	s_waitcnt lgkmcnt(0)
; #define PG8_LAS __attribute__((address_space(3)))
;     __device__ __forceinline__ void st(const void* p, const u32x4& v) const { __builtin_amdgcn_raw_buffer_store_b128(v, r, (unsigned)((const unsigned char*)p - b), 0, EPI_SC1); }
;     __device__ __forceinline__ void operator()(const f32x4 (&acc)[2][2][4][2], const Unit& u, int wr, int wc, int fr, int fq) const { const WsStore W_(wsb);
;     ...
; #pragma unroll
;                 for (int bj = 0; bj < 2; ++bj) { u32x2 w; f32x4 v0 = acc[ai][bj][m][0], v1 = acc[ai][bj][m][1];
; #pragma unroll
;                     for (int j = 0; j < 4; ++j) { asm("v_med3_f32 %0, %1, %2, %3" : "=v"(v0[j]) : "v"(v0[j]), "s"(-432.f), "v"(cl_hi)); asm("v_med3_f32 %0, %1, %2, %3" : "=v"(v1[j]) : "v"(v1[j]), "s"(-432.f), "v"(cl_hi)); }
;                     int p = 0; p = __builtin_amdgcn_cvt_pk_fp8_f32(v0[0], v0[1], p, false); p = __builtin_amdgcn_cvt_pk_fp8_f32(v0[2], v0[3], p, true); w.x = (unsigned)p;
;                     p = 0; p = __builtin_amdgcn_cvt_pk_fp8_f32(v1[0], v1[1], p, false); p = __builtin_amdgcn_cvt_pk_fp8_f32(v1[2], v1[3], p, true); w.y = (unsigned)p;
;                     *(PG8_LAS u32x2*)(stg + fr * 64 + (((bj * 4 + fq) ^ ((fr & 3) << 1)) * 8)) = w; }
;                 asm volatile("s_waitcnt lgkmcnt(0)" ::: "memory");
;                 const u32x4 w4 = *(const PG8_LAS u32x4*)(stg + rr * 64 + (((2 * ch) ^ ((rr & 3) << 1)) * 8));
;                 asm volatile("s_waitcnt lgkmcnt(0)" ::: "memory");
;                 if (FP8_ST_NT) W_.st_nt(O8 + (row0 + ai * HALF + m * 16 + rr) * 1024 + col0, w4); else W_.st(O8 + (row0 + ai * HALF + m * 16 + rr) * 1024 + col0, w4); }
	s_waitcnt lgkmcnt(0)
	buffer_store_dwordx4 v[98:101], v84, s[12:15], 0 offen nt sc1
	v_cvt_pk_fp8_f32 v75, v78, v79
	v_cvt_pk_fp8_f32 v51, v56, v54 op_sel:[0,0,1]
	v_med3_f32 v54, v42, s55, v141
	v_mov_b32_e32 v42, 0
	ds_write_b64 v124, v[90:91]
	ds_write_b64 v118, v[82:83]
	v_med3_f32 v43, v43, s55, v141
	s_waitcnt lgkmcnt(0)
	ds_read_b128 v[82:85], v140
	v_cvt_pk_fp8_f32 v42, v54, v43
	v_med3_f32 v80, v80, s55, v141
	v_med3_f32 v78, v81, s55, v141
	v_med3_f32 v44, v44, s55, v141
	v_med3_f32 v68, v68, s55, v141
	v_med3_f32 v69, v69, s55, v141
	v_med3_f32 v45, v45, s55, v141
	v_med3_f32 v35, v35, s55, v141
	s_nop 0
	v_cvt_pk_fp8_f32 v75, v80, v78 op_sel:[0,0,1]
	v_cvt_pk_fp8_f32 v66, v68, v69 op_sel:[0,0,1]
	v_cvt_pk_fp8_f32 v42, v44, v45 op_sel:[0,0,1]
	v_med3_f32 v44, v34, s55, v141
	v_mov_b32_e32 v34, 0
	v_mov_b32_e32 v59, 0
	v_cvt_pk_fp8_f32 v34, v44, v35
	v_mov_b32_e32 v35, 0
	v_add_u32_e32 v68, 0x14c08000, v119
	v_med3_f32 v62, v62, s55, v141
	v_med3_f32 v63, v63, s55, v141
	v_med3_f32 v38, v38, s55, v141
	v_med3_f32 v39, v39, s55, v141
	s_waitcnt lgkmcnt(0)
	s_waitcnt lgkmcnt(0)
	buffer_store_dwordx4 v[82:85], v68, s[12:15], 0 offen nt sc1
	v_cvt_pk_fp8_f32 v59, v62, v63
	v_cvt_pk_fp8_f32 v35, v38, v39
	ds_write_b64 v124, v[74:75]
	ds_write_b64 v118, v[66:67]
	s_waitcnt lgkmcnt(0)
	ds_read_b128 v[66:69], v140
	v_med3_f32 v38, v41, s55, v141
	v_med3_f32 v64, v64, s55, v141
	v_med3_f32 v62, v65, s55, v141
	v_med3_f32 v40, v40, s55, v141
	v_med3_f32 v52, v52, s55, v141
	v_med3_f32 v53, v53, s55, v141
	v_med3_f32 v27, v27, s55, v141
	v_mov_b32_e32 v43, 0
	v_cvt_pk_fp8_f32 v59, v64, v62 op_sel:[0,0,1]
	v_cvt_pk_fp8_f32 v35, v40, v38 op_sel:[0,0,1]
	v_med3_f32 v38, v26, s55, v141
	v_mov_b32_e32 v26, 0
	v_cvt_pk_fp8_f32 v50, v52, v53 op_sel:[0,0,1]
	v_cvt_pk_fp8_f32 v26, v38, v27
	v_add_u32_e32 v52, 0x14c0c000, v119
	v_med3_f32 v46, v46, s55, v141
	v_med3_f32 v47, v47, s55, v141
	s_waitcnt lgkmcnt(0)
	s_waitcnt lgkmcnt(0)
	buffer_store_dwordx4 v[66:69], v52, s[12:15], 0 offen nt sc1
	v_cvt_pk_fp8_f32 v43, v46, v47
	ds_write_b64 v124, v[58:59]
	ds_write_b64 v118, v[50:51]
	v_med3_f32 v28, v28, s55, v141
	s_waitcnt lgkmcnt(0)
	v_med3_f32 v29, v29, s55, v141
	v_med3_f32 v19, v19, s55, v141
	ds_read_b128 v[50:53], v140
	v_cvt_pk_fp8_f32 v26, v28, v29 op_sel:[0,0,1]
	v_med3_f32 v28, v18, s55, v141
	v_mov_b32_e32 v18, 0
	v_cvt_pk_fp8_f32 v18, v28, v19
	v_mov_b32_e32 v19, 0
	v_med3_f32 v48, v48, s55, v141
	v_med3_f32 v46, v49, s55, v141
	v_med3_f32 v22, v22, s55, v141
	v_med3_f32 v23, v23, s55, v141
	v_med3_f32 v36, v36, s55, v141
	v_med3_f32 v37, v37, s55, v141
	v_mov_b32_e32 v27, 0
	v_cvt_pk_fp8_f32 v43, v48, v46 op_sel:[0,0,1]
	v_cvt_pk_fp8_f32 v19, v22, v23
	v_cvt_pk_fp8_f32 v34, v36, v37 op_sel:[0,0,1]
	v_add_u32_e32 v36, 0x14c20000, v119
	v_med3_f32 v30, v30, s55, v141
	v_med3_f32 v31, v31, s55, v141
	v_med3_f32 v22, v25, s55, v141
	s_waitcnt lgkmcnt(0)
	s_waitcnt lgkmcnt(0)
	buffer_store_dwordx4 v[50:53], v36, s[12:15], 0 offen nt sc1
	v_cvt_pk_fp8_f32 v27, v30, v31
	ds_write_b64 v124, v[42:43]
	ds_write_b64 v118, v[34:35]
	v_med3_f32 v24, v24, s55, v141
	s_waitcnt lgkmcnt(0)
	v_med3_f32 v11, v11, s55, v141
	ds_read_b128 v[34:37], v140
	v_cvt_pk_fp8_f32 v19, v24, v22 op_sel:[0,0,1]
	v_med3_f32 v22, v10, s55, v141
	v_mov_b32_e32 v10, 0
	v_cvt_pk_fp8_f32 v10, v22, v11
	v_med3_f32 v32, v32, s55, v141
	v_med3_f32 v30, v33, s55, v141
	v_med3_f32 v20, v20, s55, v141
	v_med3_f32 v21, v21, s55, v141
	v_med3_f32 v12, v12, s55, v141
	v_mov_b32_e32 v11, 0
	v_cvt_pk_fp8_f32 v27, v32, v30 op_sel:[0,0,1]
	v_cvt_pk_fp8_f32 v18, v20, v21 op_sel:[0,0,1]
	v_med3_f32 v13, v13, s55, v141
	v_med3_f32 v3, v3, s55, v141
	v_add_u32_e32 v20, 0x14c24000, v119
	v_cvt_pk_fp8_f32 v10, v12, v13 op_sel:[0,0,1]
	v_med3_f32 v12, v2, s55, v141
	v_mov_b32_e32 v2, 0
	v_med3_f32 v14, v14, s55, v141
	v_med3_f32 v15, v15, s55, v141
	v_cvt_pk_fp8_f32 v2, v12, v3
	v_cvt_pk_fp8_f32 v11, v14, v15
	v_mov_b32_e32 v3, 0
	s_waitcnt lgkmcnt(0)
	s_waitcnt lgkmcnt(0)
	buffer_store_dwordx4 v[34:37], v20, s[12:15], 0 offen nt sc1
	ds_write_b64 v124, v[26:27]
	ds_write_b64 v118, v[18:19]
	v_med3_f32 v6, v6, s55, v141
	v_med3_f32 v7, v7, s55, v141
	s_waitcnt lgkmcnt(0)
	ds_read_b128 v[18:21], v140
	v_cvt_pk_fp8_f32 v3, v6, v7
	v_med3_f32 v16, v16, s55, v141
	v_med3_f32 v14, v17, s55, v141
	v_med3_f32 v4, v4, s55, v141
	v_med3_f32 v8, v8, s55, v141
	v_med3_f32 v5, v5, s55, v141
	v_med3_f32 v6, v9, s55, v141
	s_waitcnt lgkmcnt(0)
	s_nop 0
	v_cvt_pk_fp8_f32 v11, v16, v14 op_sel:[0,0,1]
	v_cvt_pk_fp8_f32 v2, v4, v5 op_sel:[0,0,1]
	v_cvt_pk_fp8_f32 v3, v8, v6 op_sel:[0,0,1]
	v_add_u32_e32 v4, 0x14c28000, v119
	s_waitcnt lgkmcnt(0)
	buffer_store_dwordx4 v[18:21], v4, s[12:15], 0 offen nt sc1
	ds_write_b64 v124, v[10:11]
	ds_write_b64 v118, v[2:3]
	s_waitcnt lgkmcnt(0)
	ds_read_b128 v[2:5], v140
	s_waitcnt lgkmcnt(0)
	v_add_u32_e32 v6, 0x14c2c000, v119
	s_andn2_b64 vcc, exec, s[10:11]
	s_mov_b64 s[10:11], -1
	s_waitcnt lgkmcnt(0)
	buffer_store_dwordx4 v[2:5], v6, s[12:15], 0 offen nt sc1
	s_cbranch_vccnz .LBB0_870
	s_andn2_b64 vcc, exec, s[4:5]
	s_cbranch_vccnz .LBB0_869
	s_barrier
	s_branch .LBB0_869

; __device__ __forceinline__ int crow(int r,int hi){return (r&3)+8*(r>>2)+4*hi;}
; template<int THRL> __device__ __forceinline__ void attn_unit(const bf16*Qu,const bf16*__restrict__ Kh,const bf16*__restrict__ Vh,bf16*Ou,const int NT,char*shm,const float kmax){
;     ...
;   {auto rr=__builtin_amdgcn_permlane32_swap(__float_as_uint(l_reg),__float_as_uint(l_reg),false,false);l_reg=__uint_as_float(rr[0])+__uint_as_float(rr[1]);}
;   if(hi==0)wsf[32+r32]=l_reg;asm volatile("s_waitcnt lgkmcnt(0)":::"memory");
;   float rli[16];
;   #pragma unroll
;   for(int r=0;r<16;++r)rli[r]=__builtin_amdgcn_rcpf(__builtin_fmaxf(wsf[32+crow(r,hi)],1e-30f));
;   bf16*Ow=Ou+(long)(wid*QBLK)*DMO;
;   #pragma unroll
;   for(int hf=0;hf<2;++hf){ bf16*stg=(bf16*)(shm+LDS_OST)+wid*2048;
;     #pragma unroll
;     for(int r=0;r<16;++r){const int orow=crow(r,hi);
;       #pragma unroll
;       for(int d0=0;d0<2;++d0)stg[orow*64+d0*32+r32]=__float2bfloat16(o[2*hf+d0][r]*rli[r]);}
.LBB0_1231:
	s_or_b64 exec, exec, s[0:1]
	s_waitcnt lgkmcnt(0)
	v_add_u32_e32 v74, s20, v227
	ds_read_b128 v[66:69], v74 offset:128
	ds_read_b128 v[70:73], v74 offset:160
	s_lshl_b64 s[0:1], s[14:15], 12
	s_lshl_b32 s14, s54, 7
	s_ashr_i32 s15, s14, 31
	s_waitcnt lgkmcnt(1)
	v_max_f32_e32 v66, v66, v66
	v_max_f32_e32 v66, 0xda24260, v66
	v_rcp_f32_e32 v75, v66
	v_max_f32_e32 v66, v67, v67
	v_max_f32_e32 v66, 0xda24260, v66
	v_rcp_f32_e32 v76, v66
	v_max_f32_e32 v66, v68, v68
	v_max_f32_e32 v66, 0xda24260, v66
	v_rcp_f32_e32 v77, v66
	v_max_f32_e32 v66, v69, v69
	v_max_f32_e32 v66, 0xda24260, v66
	v_rcp_f32_e32 v78, v66
	s_waitcnt lgkmcnt(0)
	v_max_f32_e32 v66, v70, v70
	v_max_f32_e32 v66, 0xda24260, v66
	v_rcp_f32_e32 v79, v66
	v_max_f32_e32 v66, v71, v71
	v_max_f32_e32 v66, 0xda24260, v66
	v_rcp_f32_e32 v80, v66
	v_max_f32_e32 v66, v72, v72
	v_max_f32_e32 v66, 0xda24260, v66
	v_rcp_f32_e32 v81, v66
	ds_read_b128 v[66:69], v74 offset:192
	v_max_f32_e32 v70, v73, v73
	v_max_f32_e32 v70, 0xda24260, v70
	v_rcp_f32_e32 v82, v70
	ds_read_b128 v[70:73], v74 offset:224
	s_waitcnt lgkmcnt(1)
	v_max_f32_e32 v66, v66, v66
	v_max_f32_e32 v66, 0xda24260, v66
	v_rcp_f32_e32 v74, v66
	v_max_f32_e32 v66, v67, v67
	v_max_f32_e32 v66, 0xda24260, v66
	v_rcp_f32_e32 v83, v66
	v_max_f32_e32 v66, v68, v68
	v_max_f32_e32 v66, 0xda24260, v66
	v_rcp_f32_e32 v68, v66
	v_max_f32_e32 v66, v69, v69
	s_add_u32 s0, s46, s0
	v_max_f32_e32 v66, 0xda24260, v66
	s_addc_u32 s1, s47, s1
	s_lshl_b32 s16, s56, 9
	v_rcp_f32_e32 v69, v66
	s_waitcnt lgkmcnt(0)
	v_max_f32_e32 v66, v70, v70
	s_add_u32 s16, s0, s16
	v_max_f32_e32 v66, 0xda24260, v66
	s_addc_u32 s17, s1, 0
	s_lshl_b64 s[0:1], s[14:15], 1
	v_rcp_f32_e32 v70, v66
	v_max_f32_e32 v66, v71, v71
	s_add_u32 s14, s16, s0
	v_max_f32_e32 v66, 0xda24260, v66
	s_addc_u32 s15, s17, s1
	v_rcp_f32_e32 v71, v66
	v_max_f32_e32 v66, v72, v72
	s_lshl_b64 s[0:1], s[12:13], 12
	v_max_f32_e32 v66, 0xda24260, v66
	s_add_u32 s0, s14, s0
	v_rcp_f32_e32 v72, v66
	v_max_f32_e32 v66, v73, v73
	s_addc_u32 s1, s15, s1
	s_lshl_b32 s12, s55, 12
	v_max_f32_e32 v66, 0xda24260, v66
	s_add_i32 s12, s12, 0
	v_rcp_f32_e32 v73, v66
	s_add_i32 s12, s12, 0x12800
	v_lshlrev_b32_e32 v66, 1, v1
	v_mul_f32_e32 v34, v34, v75
	v_add3_u32 v84, s12, v228, v66
	v_cvt_pk_bf16_f32 v34, v34, s0
	ds_write_b16 v84, v34
	v_mul_f32_e32 v34, v50, v75
	v_cvt_pk_bf16_f32 v34, v34, s0
	ds_write_b16 v84, v34 offset:64
	v_mul_f32_e32 v34, v35, v76
	v_cvt_pk_bf16_f32 v34, v34, s0
	ds_write_b16 v84, v34 offset:128
	v_mul_f32_e32 v34, v51, v76
	v_cvt_pk_bf16_f32 v34, v34, s0
	ds_write_b16 v84, v34 offset:192
	v_mul_f32_e32 v34, v36, v77
	v_cvt_pk_bf16_f32 v34, v34, s0
	ds_write_b16 v84, v34 offset:256
	v_mul_f32_e32 v34, v52, v77
	v_cvt_pk_bf16_f32 v34, v34, s0
	ds_write_b16 v84, v34 offset:320
	v_mul_f32_e32 v34, v37, v78
	v_cvt_pk_bf16_f32 v34, v34, s0
	ds_write_b16 v84, v34 offset:384
	v_mul_f32_e32 v34, v53, v78
	v_cvt_pk_bf16_f32 v34, v34, s0
	ds_write_b16 v84, v34 offset:448
	v_mul_f32_e32 v34, v38, v79
	v_cvt_pk_bf16_f32 v34, v34, s0
	ds_write_b16 v84, v34 offset:1024
	v_mul_f32_e32 v34, v54, v79
	v_cvt_pk_bf16_f32 v34, v34, s0
	ds_write_b16 v84, v34 offset:1088
	v_mul_f32_e32 v34, v39, v80
	v_cvt_pk_bf16_f32 v34, v34, s0
	ds_write_b16 v84, v34 offset:1152
	v_mul_f32_e32 v34, v55, v80
	v_cvt_pk_bf16_f32 v34, v34, s0
	ds_write_b16 v84, v34 offset:1216
	v_mul_f32_e32 v34, v40, v81
	v_cvt_pk_bf16_f32 v34, v34, s0
	ds_write_b16 v84, v34 offset:1280
	v_mul_f32_e32 v34, v56, v81
	v_cvt_pk_bf16_f32 v34, v34, s0
	ds_write_b16 v84, v34 offset:1344
	v_mul_f32_e32 v34, v41, v82
	v_cvt_pk_bf16_f32 v34, v34, s0
	ds_write_b16 v84, v34 offset:1408
	v_mul_f32_e32 v34, v57, v82
	v_cvt_pk_bf16_f32 v34, v34, s0
	ds_write_b16 v84, v34 offset:1472
	v_mul_f32_e32 v34, v42, v74
	v_cvt_pk_bf16_f32 v34, v34, s0
	ds_write_b16 v84, v34 offset:2048
	v_mul_f32_e32 v34, v58, v74
	v_cvt_pk_bf16_f32 v34, v34, s0
	ds_write_b16 v84, v34 offset:2112
	v_mul_f32_e32 v34, v43, v83
	v_cvt_pk_bf16_f32 v34, v34, s0
	ds_write_b16 v84, v34 offset:2176
	v_mul_f32_e32 v34, v59, v83
	v_cvt_pk_bf16_f32 v34, v34, s0
	ds_write_b16 v84, v34 offset:2240
	v_mul_f32_e32 v34, v44, v68
	v_cvt_pk_bf16_f32 v34, v34, s0
	ds_write_b16 v84, v34 offset:2304
	v_mul_f32_e32 v34, v60, v68
	v_cvt_pk_bf16_f32 v34, v34, s0
	ds_write_b16 v84, v34 offset:2368
	v_mul_f32_e32 v34, v45, v69
	v_cvt_pk_bf16_f32 v34, v34, s0
	ds_write_b16 v84, v34 offset:2432
	v_mul_f32_e32 v34, v61, v69
	v_cvt_pk_bf16_f32 v34, v34, s0
	ds_write_b16 v84, v34 offset:2496
	v_mul_f32_e32 v34, v46, v70
	v_cvt_pk_bf16_f32 v34, v34, s0
	ds_write_b16 v84, v34 offset:3072
	v_mul_f32_e32 v34, v62, v70
	v_cvt_pk_bf16_f32 v34, v34, s0
	ds_write_b16 v84, v34 offset:3136
	v_mul_f32_e32 v34, v47, v71
	v_cvt_pk_bf16_f32 v34, v34, s0
	ds_write_b16 v84, v34 offset:3200
	v_mul_f32_e32 v34, v63, v71
	v_cvt_pk_bf16_f32 v34, v34, s0
	ds_write_b16 v84, v34 offset:3264
	v_mul_f32_e32 v34, v48, v72
	v_cvt_pk_bf16_f32 v34, v34, s0
	ds_write_b16 v84, v34 offset:3328
	v_mul_f32_e32 v34, v64, v72
	v_cvt_pk_bf16_f32 v34, v34, s0
	ds_write_b16 v84, v34 offset:3392
	v_mul_f32_e32 v34, v49, v73
	v_cvt_pk_bf16_f32 v34, v34, s0
	ds_write_b16 v84, v34 offset:3456
	v_mul_f32_e32 v34, v65, v73
	v_cvt_pk_bf16_f32 v34, v34, s0
	v_add_u32_e32 v85, s12, v210
	ds_write_b16 v84, v34 offset:3520
	v_add_u32_e32 v86, v85, v229
	s_waitcnt lgkmcnt(0)
; __device__ __forceinline__ int crow(int r,int hi){return (r&3)+8*(r>>2)+4*hi;}
; #define ATTN_STORE16(p,v) (*(__attribute__((address_space(1))) u32x4*)(p)=(v))
; template<int THRL> __device__ __forceinline__ void attn_unit(const bf16*Qu,const bf16*__restrict__ Kh,const bf16*__restrict__ Vh,bf16*Ou,const int NT,char*shm,const float kmax){
;     ...
;   for(int hf=0;hf<2;++hf){ bf16*stg=(bf16*)(shm+LDS_OST)+wid*2048;
;     #pragma unroll
;     for(int r=0;r<16;++r){const int orow=crow(r,hi);
;       #pragma unroll
;       for(int d0=0;d0<2;++d0)stg[orow*64+d0*32+r32]=__float2bfloat16(o[2*hf+d0][r]*rli[r]);}
;     asm volatile("s_waitcnt lgkmcnt(0)":::"memory");
;     #pragma unroll
;     for(int i=0;i<4;++i){const int row=i*8+(lane>>3),ch=lane&7; const u32x4 v=*(const u32x4*)(stg+row*64+ch*8); ATTN_STORE16(Ow+(long)row*DMO+hf*64+ch*8,v);}
;     asm volatile("s_waitcnt lgkmcnt(0)":::"memory"); }
;   asm volatile("s_waitcnt lgkmcnt(0)\n\ts_barrier":::"memory");
	ds_read_b128 v[34:37], v86
	v_add_u32_e32 v48, v85, v230
	ds_read_b128 v[38:41], v48
	v_lshl_add_u64 v[66:67], s[0:1], 0, v[210:211]
	v_mov_b32_e32 v213, v211
	v_lshl_add_u64 v[42:43], v[66:67], 0, v[212:213]
	v_mov_b32_e32 v215, v211
	v_add_u32_e32 v49, v85, v231
	s_waitcnt lgkmcnt(1)
	global_store_dwordx4 v[42:43], v[34:37], off
	v_lshl_add_u64 v[44:45], v[66:67], 0, v[214:215]
	ds_read_b128 v[34:37], v49
	v_add_u32_e32 v50, v85, v232
	s_waitcnt lgkmcnt(1)
	global_store_dwordx4 v[44:45], v[38:41], off
	ds_read_b128 v[38:41], v50
	v_mov_b32_e32 v217, v211
	v_lshl_add_u64 v[46:47], v[66:67], 0, v[216:217]
	v_mov_b32_e32 v219, v211
	s_waitcnt lgkmcnt(1)
	global_store_dwordx4 v[46:47], v[34:37], off
	v_mul_f32_e32 v2, v2, v75
	v_cvt_pk_bf16_f32 v2, v2, s0
	v_lshl_add_u64 v[34:35], v[66:67], 0, v[218:219]
	s_waitcnt lgkmcnt(0)
	global_store_dwordx4 v[34:35], v[38:41], off
	s_waitcnt lgkmcnt(0)
	ds_write_b16 v84, v2
	v_mul_f32_e32 v2, v18, v75
	v_cvt_pk_bf16_f32 v2, v2, s0
	ds_write_b16 v84, v2 offset:64
	v_mul_f32_e32 v2, v3, v76
	v_cvt_pk_bf16_f32 v2, v2, s0
	ds_write_b16 v84, v2 offset:128
	v_mul_f32_e32 v2, v19, v76
	v_cvt_pk_bf16_f32 v2, v2, s0
	ds_write_b16 v84, v2 offset:192
	v_mul_f32_e32 v2, v4, v77
	v_cvt_pk_bf16_f32 v2, v2, s0
	ds_write_b16 v84, v2 offset:256
	v_mul_f32_e32 v2, v20, v77
	v_cvt_pk_bf16_f32 v2, v2, s0
	ds_write_b16 v84, v2 offset:320
	v_mul_f32_e32 v2, v5, v78
	v_cvt_pk_bf16_f32 v2, v2, s0
	ds_write_b16 v84, v2 offset:384
	v_mul_f32_e32 v2, v21, v78
	v_cvt_pk_bf16_f32 v2, v2, s0
	ds_write_b16 v84, v2 offset:448
	v_mul_f32_e32 v2, v6, v79
	v_cvt_pk_bf16_f32 v2, v2, s0
	ds_write_b16 v84, v2 offset:1024
	v_mul_f32_e32 v2, v22, v79
	v_cvt_pk_bf16_f32 v2, v2, s0
	ds_write_b16 v84, v2 offset:1088
	v_mul_f32_e32 v2, v7, v80
	v_cvt_pk_bf16_f32 v2, v2, s0
	ds_write_b16 v84, v2 offset:1152
	v_mul_f32_e32 v2, v23, v80
	v_cvt_pk_bf16_f32 v2, v2, s0
	ds_write_b16 v84, v2 offset:1216
	v_mul_f32_e32 v2, v8, v81
	v_cvt_pk_bf16_f32 v2, v2, s0
	ds_write_b16 v84, v2 offset:1280
	v_mul_f32_e32 v2, v24, v81
	v_cvt_pk_bf16_f32 v2, v2, s0
	ds_write_b16 v84, v2 offset:1344
	v_mul_f32_e32 v2, v9, v82
	v_cvt_pk_bf16_f32 v2, v2, s0
	ds_write_b16 v84, v2 offset:1408
	v_mul_f32_e32 v2, v25, v82
	v_cvt_pk_bf16_f32 v2, v2, s0
	ds_write_b16 v84, v2 offset:1472
	v_mul_f32_e32 v2, v10, v74
	v_cvt_pk_bf16_f32 v2, v2, s0
	ds_write_b16 v84, v2 offset:2048
	v_mul_f32_e32 v2, v26, v74
	v_cvt_pk_bf16_f32 v2, v2, s0
	ds_write_b16 v84, v2 offset:2112
	v_mul_f32_e32 v2, v11, v83
	v_cvt_pk_bf16_f32 v2, v2, s0
	ds_write_b16 v84, v2 offset:2176
	v_mul_f32_e32 v2, v27, v83
	v_cvt_pk_bf16_f32 v2, v2, s0
	ds_write_b16 v84, v2 offset:2240
	v_mul_f32_e32 v2, v12, v68
	v_cvt_pk_bf16_f32 v2, v2, s0
	ds_write_b16 v84, v2 offset:2304
	v_mul_f32_e32 v2, v28, v68
	v_cvt_pk_bf16_f32 v2, v2, s0
	ds_write_b16 v84, v2 offset:2368
	v_mul_f32_e32 v2, v13, v69
	v_cvt_pk_bf16_f32 v2, v2, s0
	ds_write_b16 v84, v2 offset:2432
	v_mul_f32_e32 v2, v29, v69
	v_cvt_pk_bf16_f32 v2, v2, s0
	ds_write_b16 v84, v2 offset:2496
	v_mul_f32_e32 v2, v14, v70
	v_cvt_pk_bf16_f32 v2, v2, s0
	ds_write_b16 v84, v2 offset:3072
	v_mul_f32_e32 v2, v30, v70
	v_cvt_pk_bf16_f32 v2, v2, s0
	ds_write_b16 v84, v2 offset:3136
	v_mul_f32_e32 v2, v15, v71
	v_cvt_pk_bf16_f32 v2, v2, s0
	ds_write_b16 v84, v2 offset:3200
	v_mul_f32_e32 v2, v31, v71
	v_cvt_pk_bf16_f32 v2, v2, s0
	ds_write_b16 v84, v2 offset:3264
	v_mul_f32_e32 v2, v16, v72
	v_cvt_pk_bf16_f32 v2, v2, s0
	ds_write_b16 v84, v2 offset:3328
	v_mul_f32_e32 v2, v32, v72
	v_cvt_pk_bf16_f32 v2, v2, s0
	ds_write_b16 v84, v2 offset:3392
	v_mul_f32_e32 v2, v17, v73
	v_cvt_pk_bf16_f32 v2, v2, s0
	ds_write_b16 v84, v2 offset:3456
	v_mul_f32_e32 v2, v33, v73
	v_cvt_pk_bf16_f32 v2, v2, s0
	ds_write_b16 v84, v2 offset:3520
	s_waitcnt lgkmcnt(0)
	ds_read_b128 v[2:5], v86
	ds_read_b128 v[6:9], v48
	ds_read_b128 v[10:13], v49
	ds_read_b128 v[14:17], v50
	s_waitcnt lgkmcnt(3)
	global_store_dwordx4 v[42:43], v[2:5], off offset:128
	s_waitcnt lgkmcnt(2)
	global_store_dwordx4 v[44:45], v[6:9], off offset:128
	s_waitcnt lgkmcnt(1)
	global_store_dwordx4 v[46:47], v[10:13], off offset:128
	s_waitcnt lgkmcnt(0)
	global_store_dwordx4 v[34:35], v[14:17], off offset:128
	s_waitcnt lgkmcnt(0)
	s_waitcnt lgkmcnt(0)
	s_barrier
	s_mov_b32 s12, 0

; #define PG8_LAS __attribute__((address_space(3)))
; __device__ __forceinline__ u32x4 pack8(const f32x4& a, const f32x4& b) { u32x4 w; w.x = cvt_pk_bf16(a[0], a[1]); w.y = cvt_pk_bf16(a[2], a[3]); w.z = cvt_pk_bf16(b[0], b[1]); w.w = cvt_pk_bf16(b[2], b[3]); return w; }
;     __device__ __forceinline__ void st(const void* p, const u32x4& v) const { __builtin_amdgcn_raw_buffer_store_b128(v, r, (unsigned)((const unsigned char*)p - b), 0, EPI_SC1); }
;     __device__ __forceinline__ void operator()(const f32x4 (&acc)[2][2][4][2], const Unit& u, int wr, int wc, int fr, int fq) const { const WsStore W_(wsb);
;     ...
;         PG8_LAS unsigned char* stg = stg0 + (wr * 4 + wc) * 2048;
;         const int lane = fr + 16 * fq, rr = lane >> 3, ch = lane & 7;
;         const int row0 = u.pm * BM + wr * 64, col0 = coff + u.pn * BM + wc * 64 + ch * 8;
; #pragma unroll
;         for (int ai = 0; ai < 2; ++ai)
; #pragma unroll
;             for (int m = 0; m < 4; ++m) {
;                 if (EPI_DIRECT) {
; #pragma unroll
;                     for (int bj = 0; bj < 2; ++bj) W_.st(O + (size_t)(row0 + ai * HALF + m * 16 + fr) * ldc + coff + u.pn * BM + wc * 64 + bj * 32 + 8 * fq, pack8(acc[ai][bj][m][0], acc[ai][bj][m][1]));
;                     continue; }
; #pragma unroll
;                 for (int bj = 0; bj < 2; ++bj) *(PG8_LAS u32x4*)(stg + fr * 128 + (((bj * 4 + fq) ^ (fr & 7)) * 16)) = pack8(acc[ai][bj][m][0], acc[ai][bj][m][1]);
;                 asm volatile("s_waitcnt lgkmcnt(0)" ::: "memory");
;                 u32x4 w[2];
; #pragma unroll
;                 for (int r = 0; r < 2; ++r) { const int row = 8 * r + rr; w[r] = *(const PG8_LAS u32x4*)(stg + row * 128 + ((ch ^ (row & 7)) * 16)); }
;                 asm volatile("s_waitcnt lgkmcnt(0)" ::: "memory");
; #pragma unroll
;                 for (int r = 0; r < 2; ++r) W_.st(O + (size_t)(row0 + ai * HALF + m * 16 + 8 * r + rr) * ldc + col0, w[r]); }
.LBB0_1386:
	v_mov_b32_e32 v144, v0
	v_cvt_pk_bf16_f32 v126, v126, v127
	v_cvt_pk_bf16_f32 v127, v128, v129
	v_cvt_pk_bf16_f32 v128, v118, v119
	v_cvt_pk_bf16_f32 v129, v120, v121
	s_andn2_b64 vcc, exec, s[2:3]
	v_readfirstlane_b32 s16, v144
	s_ashr_i32 s17, s16, 8
	s_bfe_u32 s16, s16, 0x20006
	s_lshl_b32 s30, s17, 13
	s_lshl_b32 s31, s16, 11
	s_add_i32 s30, s30, 0
	s_add_i32 s30, s30, s31
	v_lshlrev_b32_e32 v151, 7, v144
	v_lshrrev_b32_e32 v145, 4, v144
	s_add_i32 s30, s30, 0x22000
	v_and_b32_e32 v149, 7, v144
	v_and_b32_e32 v151, 0x780, v151
	v_add_u32_e32 v151, s30, v151
	v_bitop3_b32 v118, v145, v149, 3 bitop3:0x6c
	v_bfe_u32 v146, v144, 4, 2
	v_lshl_add_u32 v145, v118, 4, v151
	v_lshrrev_b32_e32 v147, 3, v144
	ds_write_b128 v145, v[126:129]
	v_cvt_pk_bf16_f32 v118, v122, v123
	v_cvt_pk_bf16_f32 v119, v124, v125
	v_cvt_pk_bf16_f32 v120, v114, v115
	v_bitop3_b32 v114, v146, v149, 4 bitop3:0x36
	v_bfe_u32 v148, v144, 3, 3
	v_bitop3_b32 v144, v147, v144, 7 bitop3:0x28
	v_lshl_add_u32 v122, v114, 4, v151
	s_lshl_b32 s31, s57, 8
	s_lshl_b32 s17, s17, 6
	v_lshlrev_b32_e32 v152, 7, v148
	v_lshlrev_b32_e32 v144, 4, v144
	v_cvt_pk_bf16_f32 v121, v116, v117
	ds_write_b128 v122, v[118:121]
	s_add_i32 s17, s17, s31
	s_lshl_b32 s31, s56, 9
	v_add3_u32 v144, s30, v152, v144
	s_waitcnt lgkmcnt(0)
	v_lshl_or_b32 v150, v149, 4, s31
	ds_read_b128 v[114:117], v144
	ds_read_b128 v[118:121], v144 offset:1024
	v_lshl_or_b32 v150, s16, 7, v150
	v_or_b32_e32 v147, s17, v148
	v_lshl_add_u32 v123, v147, 11, v150
	v_add_u32_e32 v124, 0x19000000, v123
	s_waitcnt lgkmcnt(0)
	s_waitcnt lgkmcnt(0)
	buffer_store_dwordx4 v[114:117], v124, s[12:15], 0 offen sc1
	s_mov_b64 s[2:3], -1
	s_nop 0
	v_add_u32_e32 v114, 0x19004000, v123
	buffer_store_dwordx4 v[118:121], v114, s[12:15], 0 offen sc1
	v_cvt_pk_bf16_f32 v106, v106, v107
	v_cvt_pk_bf16_f32 v107, v108, v109
	v_cvt_pk_bf16_f32 v108, v98, v99
	v_cvt_pk_bf16_f32 v109, v100, v101
	ds_write_b128 v145, v[106:109]
	v_cvt_pk_bf16_f32 v98, v110, v111
	v_cvt_pk_bf16_f32 v99, v112, v113
	v_cvt_pk_bf16_f32 v100, v102, v103
	v_cvt_pk_bf16_f32 v101, v104, v105
	ds_write_b128 v122, v[98:101]
	s_waitcnt lgkmcnt(0)
	ds_read_b128 v[98:101], v144
	ds_read_b128 v[102:105], v144 offset:1024
	v_add_u32_e32 v106, 0x19008000, v123
	s_waitcnt lgkmcnt(0)
	s_waitcnt lgkmcnt(0)
	buffer_store_dwordx4 v[98:101], v106, s[12:15], 0 offen sc1
	s_nop 1
	v_add_u32_e32 v98, 0x1900c000, v123
	buffer_store_dwordx4 v[102:105], v98, s[12:15], 0 offen sc1
	v_cvt_pk_bf16_f32 v90, v90, v91
	v_cvt_pk_bf16_f32 v91, v92, v93
	v_cvt_pk_bf16_f32 v92, v82, v83
	v_cvt_pk_bf16_f32 v93, v84, v85
	ds_write_b128 v145, v[90:93]
	v_cvt_pk_bf16_f32 v82, v94, v95
	v_cvt_pk_bf16_f32 v83, v96, v97
	v_cvt_pk_bf16_f32 v84, v86, v87
	v_cvt_pk_bf16_f32 v85, v88, v89
	ds_write_b128 v122, v[82:85]
	s_waitcnt lgkmcnt(0)
	ds_read_b128 v[82:85], v144
	ds_read_b128 v[86:89], v144 offset:1024
	v_add_u32_e32 v90, 0x19010000, v123
	s_waitcnt lgkmcnt(0)
	s_waitcnt lgkmcnt(0)
	buffer_store_dwordx4 v[82:85], v90, s[12:15], 0 offen sc1
	s_nop 1
	v_add_u32_e32 v82, 0x19014000, v123
	buffer_store_dwordx4 v[86:89], v82, s[12:15], 0 offen sc1
	v_cvt_pk_bf16_f32 v58, v58, v59
	v_cvt_pk_bf16_f32 v59, v60, v61
	v_cvt_pk_bf16_f32 v60, v50, v51
	v_cvt_pk_bf16_f32 v61, v52, v53
	ds_write_b128 v145, v[58:61]
	v_cvt_pk_bf16_f32 v50, v62, v63
	v_cvt_pk_bf16_f32 v51, v64, v65
	v_cvt_pk_bf16_f32 v52, v54, v55
	v_cvt_pk_bf16_f32 v53, v56, v57
	ds_write_b128 v122, v[50:53]
	s_waitcnt lgkmcnt(0)
	ds_read_b128 v[50:53], v144
	ds_read_b128 v[54:57], v144 offset:1024
	v_add_u32_e32 v58, 0x19018000, v123
	s_waitcnt lgkmcnt(0)
	s_waitcnt lgkmcnt(0)
	buffer_store_dwordx4 v[50:53], v58, s[12:15], 0 offen sc1
	v_add_u32_e32 v58, 0x19040000, v123
	s_nop 0
	v_add_u32_e32 v50, 0x1901c000, v123
	buffer_store_dwordx4 v[54:57], v50, s[12:15], 0 offen sc1
	v_cvt_pk_bf16_f32 v50, v74, v75
	v_cvt_pk_bf16_f32 v51, v76, v77
	v_cvt_pk_bf16_f32 v52, v66, v67
	v_cvt_pk_bf16_f32 v53, v68, v69
	ds_write_b128 v145, v[50:53]
	v_cvt_pk_bf16_f32 v50, v78, v79
	v_cvt_pk_bf16_f32 v51, v80, v81
	v_cvt_pk_bf16_f32 v52, v70, v71
	v_cvt_pk_bf16_f32 v53, v72, v73
	ds_write_b128 v122, v[50:53]
	s_waitcnt lgkmcnt(0)
	ds_read_b128 v[50:53], v144
	ds_read_b128 v[54:57], v144 offset:1024
	s_waitcnt lgkmcnt(0)
	s_waitcnt lgkmcnt(0)
	buffer_store_dwordx4 v[50:53], v58, s[12:15], 0 offen sc1
	s_nop 1
	v_add_u32_e32 v50, 0x19044000, v123
	buffer_store_dwordx4 v[54:57], v50, s[12:15], 0 offen sc1
	v_cvt_pk_bf16_f32 v42, v42, v43
	v_cvt_pk_bf16_f32 v43, v44, v45
	v_cvt_pk_bf16_f32 v44, v34, v35
	v_cvt_pk_bf16_f32 v45, v36, v37
	ds_write_b128 v145, v[42:45]
	v_cvt_pk_bf16_f32 v34, v46, v47
	v_cvt_pk_bf16_f32 v35, v48, v49
	v_cvt_pk_bf16_f32 v36, v38, v39
	v_cvt_pk_bf16_f32 v37, v40, v41
	ds_write_b128 v122, v[34:37]
	s_waitcnt lgkmcnt(0)
	ds_read_b128 v[34:37], v144
	ds_read_b128 v[38:41], v144 offset:1024
	v_add_u32_e32 v42, 0x19048000, v123
	s_waitcnt lgkmcnt(0)
	s_waitcnt lgkmcnt(0)
	buffer_store_dwordx4 v[34:37], v42, s[12:15], 0 offen sc1
	s_nop 1
	v_add_u32_e32 v34, 0x1904c000, v123
	buffer_store_dwordx4 v[38:41], v34, s[12:15], 0 offen sc1
	v_cvt_pk_bf16_f32 v26, v26, v27
	v_cvt_pk_bf16_f32 v27, v28, v29
	v_cvt_pk_bf16_f32 v28, v18, v19
	v_cvt_pk_bf16_f32 v29, v20, v21
	ds_write_b128 v145, v[26:29]
	v_cvt_pk_bf16_f32 v18, v30, v31
	v_cvt_pk_bf16_f32 v19, v32, v33
	v_cvt_pk_bf16_f32 v20, v22, v23
	v_cvt_pk_bf16_f32 v21, v24, v25
	ds_write_b128 v122, v[18:21]
	s_waitcnt lgkmcnt(0)
	ds_read_b128 v[18:21], v144
	ds_read_b128 v[22:25], v144 offset:1024
	v_add_u32_e32 v26, 0x19050000, v123
	s_waitcnt lgkmcnt(0)
	s_waitcnt lgkmcnt(0)
	buffer_store_dwordx4 v[18:21], v26, s[12:15], 0 offen sc1
	s_nop 1
	v_add_u32_e32 v18, 0x19054000, v123
	buffer_store_dwordx4 v[22:25], v18, s[12:15], 0 offen sc1
	v_cvt_pk_bf16_f32 v10, v10, v11
	v_cvt_pk_bf16_f32 v11, v12, v13
	v_cvt_pk_bf16_f32 v12, v2, v3
	v_cvt_pk_bf16_f32 v13, v4, v5
	ds_write_b128 v145, v[10:13]
	v_cvt_pk_bf16_f32 v2, v14, v15
	v_cvt_pk_bf16_f32 v3, v16, v17
	v_cvt_pk_bf16_f32 v4, v6, v7
	v_cvt_pk_bf16_f32 v5, v8, v9
	ds_write_b128 v122, v[2:5]
	s_waitcnt lgkmcnt(0)
	ds_read_b128 v[2:5], v144
	ds_read_b128 v[6:9], v144 offset:1024
	s_waitcnt lgkmcnt(0)
	v_add_u32_e32 v10, 0x19058000, v123
	s_waitcnt lgkmcnt(0)
	buffer_store_dwordx4 v[2:5], v10, s[12:15], 0 offen sc1
	s_nop 1
	v_add_u32_e32 v2, 0x1905c000, v123
	buffer_store_dwordx4 v[6:9], v2, s[12:15], 0 offen sc1
	s_cbranch_vccnz .LBB0_1375
	s_andn2_b64 vcc, exec, s[4:5]
	s_cbranch_vccnz .LBB0_1374
	s_barrier
	s_branch .LBB0_1374

; #define PG8_LAS __attribute__((address_space(3)))
;     __device__ __forceinline__ void st(const void* p, const u32x4& v) const { __builtin_amdgcn_raw_buffer_store_b128(v, r, (unsigned)((const unsigned char*)p - b), 0, EPI_SC1); }
;     __device__ __forceinline__ void operator()(const f32x4 (&acc)[2][2][4][2], const Unit& u, int wr, int wc, int fr, int fq) const { const WsStore W_(wsb);
;     ...
;         PG8_LAS unsigned char* stg = stg0 + (wr * 4 + wc) * 2048;
;         const int lane = fr + 16 * fq, rr = lane >> 2, ch = lane & 3;
;         const size_t row0 = (size_t)u.pm * BM + wr * 64; const int col0 = u.pn * BM + wc * 64 + ch * 16;
;         float cl_hi = 432.f; asm volatile("" : "+v"(cl_hi));
; #pragma unroll
;         for (int ai = 0; ai < 2; ++ai)
; #pragma unroll
;             for (int m = 0; m < 4; ++m) {
; #pragma unroll
;                 for (int bj = 0; bj < 2; ++bj) { u32x2 w; f32x4 v0 = acc[ai][bj][m][0], v1 = acc[ai][bj][m][1];
; #pragma unroll
;                     for (int j = 0; j < 4; ++j) { asm("v_med3_f32 %0, %1, %2, %3" : "=v"(v0[j]) : "v"(v0[j]), "s"(-432.f), "v"(cl_hi)); asm("v_med3_f32 %0, %1, %2, %3" : "=v"(v1[j]) : "v"(v1[j]), "s"(-432.f), "v"(cl_hi)); }
;                     int p = 0; p = __builtin_amdgcn_cvt_pk_fp8_f32(v0[0], v0[1], p, false); p = __builtin_amdgcn_cvt_pk_fp8_f32(v0[2], v0[3], p, true); w.x = (unsigned)p;
;                     p = 0; p = __builtin_amdgcn_cvt_pk_fp8_f32(v1[0], v1[1], p, false); p = __builtin_amdgcn_cvt_pk_fp8_f32(v1[2], v1[3], p, true); w.y = (unsigned)p;
;                     *(PG8_LAS u32x2*)(stg + fr * 64 + (((bj * 4 + fq) ^ ((fr & 3) << 1)) * 8)) = w; }
;                 asm volatile("s_waitcnt lgkmcnt(0)" ::: "memory");
;                 const u32x4 w4 = *(const PG8_LAS u32x4*)(stg + rr * 64 + (((2 * ch) ^ ((rr & 3) << 1)) * 8));
;                 asm volatile("s_waitcnt lgkmcnt(0)" ::: "memory");
;                 if (FP8_ST_NT) W_.st_nt(O8 + (row0 + ai * HALF + m * 16 + rr) * 1024 + col0, w4); else W_.st(O8 + (row0 + ai * HALF + m * 16 + rr) * 1024 + col0, w4); }
.LBB0_1731:
	v_mov_b32_e32 v140, v0
	s_lshl_b32 s57, s57, 8
	v_readfirstlane_b32 s30, v140
	s_ashr_i32 s31, s30, 8
	s_bfe_u32 s30, s30, 0x20006
	s_lshl_b32 s59, s31, 13
	s_lshl_b32 s31, s31, 6
	s_lshl_b32 s60, s30, 11
	s_add_i32 s31, s31, s57
	s_lshl_b32 s57, s58, 8
	s_lshl_b32 s30, s30, 6
	s_or_b32 s30, s30, s57
	v_lshlrev_b32_e32 v141, 4, v140
	v_lshrrev_b32_e32 v144, 2, v140
	v_bfe_u32 v145, v140, 2, 4
	v_and_or_b32 v146, v141, 48, s30
	v_mov_b32_e32 v141, 0x43d80000
	v_and_b32_e32 v142, 15, v140
	v_bfe_u32 v143, v140, 4, 2
	v_lshlrev_b32_e32 v147, 1, v140
	v_lshlrev_b32_e32 v149, 6, v145
	v_xor_b32_e32 v140, v144, v140
	v_or_b32_e32 v144, s31, v145
	v_med3_f32 v145, v122, s54, v141
	v_mov_b32_e32 v122, 0
	v_med3_f32 v123, v123, s54, v141
	v_med3_f32 v125, v125, s54, v141
	v_med3_f32 v124, v124, s54, v141
	v_med3_f32 v115, v115, s54, v141
	v_med3_f32 v118, v118, s54, v141
	v_med3_f32 v119, v119, s54, v141
	s_nop 0
	v_cvt_pk_fp8_f32 v122, v145, v123
	v_med3_f32 v120, v120, s54, v141
	v_med3_f32 v107, v107, s54, v141
	v_med3_f32 v108, v108, s54, v141
	v_cvt_pk_fp8_f32 v122, v124, v125 op_sel:[0,0,1]
	v_med3_f32 v125, v114, s54, v141
	v_mov_b32_e32 v114, 0
	v_cvt_pk_fp8_f32 v114, v125, v115
	v_mov_b32_e32 v115, 0
	v_cvt_pk_fp8_f32 v115, v118, v119
	v_med3_f32 v118, v121, s54, v141
	v_med3_f32 v109, v109, s54, v141
	v_med3_f32 v99, v99, s54, v141
	v_med3_f32 v102, v102, s54, v141
	v_med3_f32 v103, v103, s54, v141
	v_med3_f32 v104, v104, s54, v141
	s_nop 0
	v_cvt_pk_fp8_f32 v115, v120, v118 op_sel:[0,0,1]
	v_med3_f32 v120, v106, s54, v141
	v_mov_b32_e32 v106, 0
	v_cvt_pk_fp8_f32 v106, v120, v107
	v_med3_f32 v91, v91, s54, v141
	v_med3_f32 v92, v92, s54, v141
	v_med3_f32 v93, v93, s54, v141
	v_cvt_pk_fp8_f32 v106, v108, v109 op_sel:[0,0,1]
	v_med3_f32 v108, v98, s54, v141
	v_mov_b32_e32 v98, 0
	v_cvt_pk_fp8_f32 v98, v108, v99
	v_mov_b32_e32 v99, 0
	v_cvt_pk_fp8_f32 v99, v102, v103
	v_med3_f32 v102, v105, s54, v141
	v_med3_f32 v83, v83, s54, v141
	v_med3_f32 v86, v86, s54, v141
	v_med3_f32 v87, v87, s54, v141
	v_mov_b32_e32 v123, 0
	v_cvt_pk_fp8_f32 v99, v104, v102 op_sel:[0,0,1]
	v_med3_f32 v102, v90, s54, v141
	v_mov_b32_e32 v90, 0
	v_cvt_pk_fp8_f32 v90, v102, v91
	v_med3_f32 v88, v88, s54, v141
	v_med3_f32 v126, v126, s54, v141
	v_med3_f32 v127, v127, s54, v141
	v_cvt_pk_fp8_f32 v90, v92, v93 op_sel:[0,0,1]
	v_med3_f32 v92, v82, s54, v141
	v_mov_b32_e32 v82, 0
	v_cvt_pk_fp8_f32 v82, v92, v83
	v_mov_b32_e32 v83, 0
	v_cvt_pk_fp8_f32 v83, v86, v87
	v_med3_f32 v86, v89, s54, v141
	v_cvt_pk_fp8_f32 v123, v126, v127
	v_med3_f32 v75, v75, s54, v141
	v_cvt_pk_fp8_f32 v83, v88, v86 op_sel:[0,0,1]
	v_med3_f32 v86, v74, s54, v141
	v_mov_b32_e32 v74, 0
	v_cvt_pk_fp8_f32 v74, v86, v75
	s_add_i32 s59, s59, 0
	v_med3_f32 v76, v76, s54, v141
	s_add_i32 s59, s59, s60
	v_med3_f32 v128, v128, s54, v141
	v_med3_f32 v126, v129, s54, v141
	v_med3_f32 v116, v116, s54, v141
	v_med3_f32 v117, v117, s54, v141
	v_med3_f32 v77, v77, s54, v141
	v_med3_f32 v67, v67, s54, v141
	s_add_i32 s59, s59, 0x22000
	v_cvt_pk_fp8_f32 v123, v128, v126 op_sel:[0,0,1]
	v_cvt_pk_fp8_f32 v114, v116, v117 op_sel:[0,0,1]
	v_cvt_pk_fp8_f32 v74, v76, v77 op_sel:[0,0,1]
	v_med3_f32 v76, v66, s54, v141
	v_mov_b32_e32 v66, 0
	v_and_b32_e32 v148, 6, v147
	v_cvt_pk_fp8_f32 v66, v76, v67
	v_mov_b32_e32 v67, 0
	v_lshl_add_u32 v142, v142, 6, s59
	v_bitop3_b32 v124, v147, v143, 6 bitop3:0x6c
	v_bitop3_b32 v116, v143, v148, 4 bitop3:0x36
	v_mov_b32_e32 v107, 0
	v_med3_f32 v70, v70, s54, v141
	v_med3_f32 v71, v71, s54, v141
	v_lshlrev_b32_e32 v140, 4, v140
	v_cvt_pk_fp8_f32 v67, v70, v71
	v_lshl_add_u32 v124, v124, 3, v142
	v_lshl_add_u32 v118, v116, 3, v142
	v_med3_f32 v110, v110, s54, v141
	v_med3_f32 v111, v111, s54, v141
	v_and_b32_e32 v140, 48, v140
	v_cvt_pk_fp8_f32 v107, v110, v111
	ds_write_b64 v124, v[122:123]
	ds_write_b64 v118, v[114:115]
	v_add3_u32 v140, s59, v149, v140
	s_waitcnt lgkmcnt(0)
	v_med3_f32 v70, v73, s54, v141
	ds_read_b128 v[114:117], v140
	v_med3_f32 v72, v72, s54, v141
	v_med3_f32 v112, v112, s54, v141
	v_med3_f32 v110, v113, s54, v141
	v_med3_f32 v59, v59, s54, v141
	v_med3_f32 v100, v100, s54, v141
	v_med3_f32 v101, v101, s54, v141
	s_nop 0
	v_cvt_pk_fp8_f32 v67, v72, v70 op_sel:[0,0,1]
	v_med3_f32 v70, v58, s54, v141
	v_mov_b32_e32 v58, 0
	v_cvt_pk_fp8_f32 v107, v112, v110 op_sel:[0,0,1]
	v_cvt_pk_fp8_f32 v58, v70, v59
	v_cvt_pk_fp8_f32 v98, v100, v101 op_sel:[0,0,1]
	v_lshl_add_u32 v119, v144, 10, v146
	v_mov_b32_e32 v91, 0
	v_add_u32_e32 v100, 0x14c00000, v119
	v_med3_f32 v94, v94, s54, v141
	v_med3_f32 v95, v95, s54, v141
	v_med3_f32 v60, v60, s54, v141
	s_waitcnt lgkmcnt(0)
	s_waitcnt lgkmcnt(0)
	buffer_store_dwordx4 v[114:117], v100, s[8:11], 0 offen nt sc1
	v_cvt_pk_fp8_f32 v91, v94, v95
	ds_write_b64 v124, v[106:107]
	ds_write_b64 v118, v[98:99]
	v_med3_f32 v61, v61, s54, v141
	v_med3_f32 v51, v51, s54, v141
	s_waitcnt lgkmcnt(0)
	ds_read_b128 v[98:101], v140
	v_cvt_pk_fp8_f32 v58, v60, v61 op_sel:[0,0,1]
	v_med3_f32 v60, v50, s54, v141
	v_mov_b32_e32 v50, 0
	v_cvt_pk_fp8_f32 v50, v60, v51
	v_mov_b32_e32 v51, 0
	v_med3_f32 v54, v54, s54, v141
	v_med3_f32 v55, v55, s54, v141
	v_med3_f32 v96, v96, s54, v141
	v_med3_f32 v94, v97, s54, v141
	v_med3_f32 v84, v84, s54, v141
	v_med3_f32 v85, v85, s54, v141
	v_mov_b32_e32 v75, 0
	v_cvt_pk_fp8_f32 v51, v54, v55
	v_cvt_pk_fp8_f32 v91, v96, v94 op_sel:[0,0,1]
	v_cvt_pk_fp8_f32 v82, v84, v85 op_sel:[0,0,1]
	v_med3_f32 v54, v57, s54, v141
	v_add_u32_e32 v84, 0x14c04000, v119
	v_med3_f32 v78, v78, s54, v141
	v_med3_f32 v79, v79, s54, v141
	v_med3_f32 v56, v56, s54, v141
	s_waitcnt lgkmcnt(0)
; #define PG8_LAS __attribute__((address_space(3)))
;     __device__ __forceinline__ void st(const void* p, const u32x4& v) const { __builtin_amdgcn_raw_buffer_store_b128(v, r, (unsigned)((const unsigned char*)p - b), 0, EPI_SC1); }
;     __device__ __forceinline__ void operator()(const f32x4 (&acc)[2][2][4][2], const Unit& u, int wr, int wc, int fr, int fq) const { const WsStore W_(wsb);
;     ...
; #pragma unroll
;                 for (int bj = 0; bj < 2; ++bj) { u32x2 w; f32x4 v0 = acc[ai][bj][m][0], v1 = acc[ai][bj][m][1];
; #pragma unroll
;                     for (int j = 0; j < 4; ++j) { asm("v_med3_f32 %0, %1, %2, %3" : "=v"(v0[j]) : "v"(v0[j]), "s"(-432.f), "v"(cl_hi)); asm("v_med3_f32 %0, %1, %2, %3" : "=v"(v1[j]) : "v"(v1[j]), "s"(-432.f), "v"(cl_hi)); }
;                     int p = 0; p = __builtin_amdgcn_cvt_pk_fp8_f32(v0[0], v0[1], p, false); p = __builtin_amdgcn_cvt_pk_fp8_f32(v0[2], v0[3], p, true); w.x = (unsigned)p;
;                     p = 0; p = __builtin_amdgcn_cvt_pk_fp8_f32(v1[0], v1[1], p, false); p = __builtin_amdgcn_cvt_pk_fp8_f32(v1[2], v1[3], p, true); w.y = (unsigned)p;
;                     *(PG8_LAS u32x2*)(stg + fr * 64 + (((bj * 4 + fq) ^ ((fr & 3) << 1)) * 8)) = w; }
;                 asm volatile("s_waitcnt lgkmcnt(0)" ::: "memory");
;                 const u32x4 w4 = *(const PG8_LAS u32x4*)(stg + rr * 64 + (((2 * ch) ^ ((rr & 3) << 1)) * 8));
;                 asm volatile("s_waitcnt lgkmcnt(0)" ::: "memory");
;                 if (FP8_ST_NT) W_.st_nt(O8 + (row0 + ai * HALF + m * 16 + rr) * 1024 + col0, w4); else W_.st(O8 + (row0 + ai * HALF + m * 16 + rr) * 1024 + col0, w4); }
	s_waitcnt lgkmcnt(0)
	buffer_store_dwordx4 v[98:101], v84, s[8:11], 0 offen nt sc1
	v_cvt_pk_fp8_f32 v75, v78, v79
	v_cvt_pk_fp8_f32 v51, v56, v54 op_sel:[0,0,1]
	v_med3_f32 v54, v42, s54, v141
	v_mov_b32_e32 v42, 0
	ds_write_b64 v124, v[90:91]
	ds_write_b64 v118, v[82:83]
	v_med3_f32 v43, v43, s54, v141
	s_waitcnt lgkmcnt(0)
	ds_read_b128 v[82:85], v140
	v_cvt_pk_fp8_f32 v42, v54, v43
	v_med3_f32 v80, v80, s54, v141
	v_med3_f32 v78, v81, s54, v141
	v_med3_f32 v44, v44, s54, v141
	v_med3_f32 v68, v68, s54, v141
	v_med3_f32 v69, v69, s54, v141
	v_med3_f32 v45, v45, s54, v141
	v_med3_f32 v35, v35, s54, v141
	s_nop 0
	v_cvt_pk_fp8_f32 v75, v80, v78 op_sel:[0,0,1]
	v_cvt_pk_fp8_f32 v66, v68, v69 op_sel:[0,0,1]
	v_cvt_pk_fp8_f32 v42, v44, v45 op_sel:[0,0,1]
	v_med3_f32 v44, v34, s54, v141
	v_mov_b32_e32 v34, 0
	v_mov_b32_e32 v59, 0
	v_cvt_pk_fp8_f32 v34, v44, v35
	v_mov_b32_e32 v35, 0
	v_add_u32_e32 v68, 0x14c08000, v119
	v_med3_f32 v62, v62, s54, v141
	v_med3_f32 v63, v63, s54, v141
	v_med3_f32 v38, v38, s54, v141
	v_med3_f32 v39, v39, s54, v141
	s_waitcnt lgkmcnt(0)
	s_waitcnt lgkmcnt(0)
	buffer_store_dwordx4 v[82:85], v68, s[8:11], 0 offen nt sc1
	v_cvt_pk_fp8_f32 v59, v62, v63
	v_cvt_pk_fp8_f32 v35, v38, v39
	ds_write_b64 v124, v[74:75]
	ds_write_b64 v118, v[66:67]
	s_waitcnt lgkmcnt(0)
	ds_read_b128 v[66:69], v140
	v_med3_f32 v38, v41, s54, v141
	v_med3_f32 v64, v64, s54, v141
	v_med3_f32 v62, v65, s54, v141
	v_med3_f32 v40, v40, s54, v141
	v_med3_f32 v52, v52, s54, v141
	v_med3_f32 v53, v53, s54, v141
	v_med3_f32 v27, v27, s54, v141
	v_mov_b32_e32 v43, 0
	v_cvt_pk_fp8_f32 v59, v64, v62 op_sel:[0,0,1]
	v_cvt_pk_fp8_f32 v35, v40, v38 op_sel:[0,0,1]
	v_med3_f32 v38, v26, s54, v141
	v_mov_b32_e32 v26, 0
	v_cvt_pk_fp8_f32 v50, v52, v53 op_sel:[0,0,1]
	v_cvt_pk_fp8_f32 v26, v38, v27
	v_add_u32_e32 v52, 0x14c0c000, v119
	v_med3_f32 v46, v46, s54, v141
	v_med3_f32 v47, v47, s54, v141
	s_waitcnt lgkmcnt(0)
	s_waitcnt lgkmcnt(0)
	buffer_store_dwordx4 v[66:69], v52, s[8:11], 0 offen nt sc1
	v_cvt_pk_fp8_f32 v43, v46, v47
	ds_write_b64 v124, v[58:59]
	ds_write_b64 v118, v[50:51]
	v_med3_f32 v28, v28, s54, v141
	s_waitcnt lgkmcnt(0)
	v_med3_f32 v29, v29, s54, v141
	v_med3_f32 v19, v19, s54, v141
	ds_read_b128 v[50:53], v140
	v_cvt_pk_fp8_f32 v26, v28, v29 op_sel:[0,0,1]
	v_med3_f32 v28, v18, s54, v141
	v_mov_b32_e32 v18, 0
	v_cvt_pk_fp8_f32 v18, v28, v19
	v_mov_b32_e32 v19, 0
	v_med3_f32 v48, v48, s54, v141
	v_med3_f32 v46, v49, s54, v141
	v_med3_f32 v22, v22, s54, v141
	v_med3_f32 v23, v23, s54, v141
	v_med3_f32 v36, v36, s54, v141
	v_med3_f32 v37, v37, s54, v141
	v_mov_b32_e32 v27, 0
	v_cvt_pk_fp8_f32 v43, v48, v46 op_sel:[0,0,1]
	v_cvt_pk_fp8_f32 v19, v22, v23
	v_cvt_pk_fp8_f32 v34, v36, v37 op_sel:[0,0,1]
	v_add_u32_e32 v36, 0x14c20000, v119
	v_med3_f32 v30, v30, s54, v141
	v_med3_f32 v31, v31, s54, v141
	v_med3_f32 v22, v25, s54, v141
	s_waitcnt lgkmcnt(0)
	s_waitcnt lgkmcnt(0)
	buffer_store_dwordx4 v[50:53], v36, s[8:11], 0 offen nt sc1
	v_cvt_pk_fp8_f32 v27, v30, v31
	ds_write_b64 v124, v[42:43]
	ds_write_b64 v118, v[34:35]
	v_med3_f32 v24, v24, s54, v141
	s_waitcnt lgkmcnt(0)
	v_med3_f32 v11, v11, s54, v141
	ds_read_b128 v[34:37], v140
	v_cvt_pk_fp8_f32 v19, v24, v22 op_sel:[0,0,1]
	v_med3_f32 v22, v10, s54, v141
	v_mov_b32_e32 v10, 0
	v_cvt_pk_fp8_f32 v10, v22, v11
	v_med3_f32 v32, v32, s54, v141
	v_med3_f32 v30, v33, s54, v141
	v_med3_f32 v20, v20, s54, v141
	v_med3_f32 v21, v21, s54, v141
	v_med3_f32 v12, v12, s54, v141
	v_mov_b32_e32 v11, 0
	v_cvt_pk_fp8_f32 v27, v32, v30 op_sel:[0,0,1]
	v_cvt_pk_fp8_f32 v18, v20, v21 op_sel:[0,0,1]
	v_med3_f32 v13, v13, s54, v141
	v_med3_f32 v3, v3, s54, v141
	v_add_u32_e32 v20, 0x14c24000, v119
	v_cvt_pk_fp8_f32 v10, v12, v13 op_sel:[0,0,1]
	v_med3_f32 v12, v2, s54, v141
	v_mov_b32_e32 v2, 0
	v_med3_f32 v14, v14, s54, v141
	v_med3_f32 v15, v15, s54, v141
	v_cvt_pk_fp8_f32 v2, v12, v3
	v_cvt_pk_fp8_f32 v11, v14, v15
	v_mov_b32_e32 v3, 0
	s_waitcnt lgkmcnt(0)
	s_waitcnt lgkmcnt(0)
	buffer_store_dwordx4 v[34:37], v20, s[8:11], 0 offen nt sc1
	ds_write_b64 v124, v[26:27]
	ds_write_b64 v118, v[18:19]
	v_med3_f32 v6, v6, s54, v141
	v_med3_f32 v7, v7, s54, v141
	s_waitcnt lgkmcnt(0)
	ds_read_b128 v[18:21], v140
	v_cvt_pk_fp8_f32 v3, v6, v7
	v_med3_f32 v16, v16, s54, v141
	v_med3_f32 v14, v17, s54, v141
	v_med3_f32 v4, v4, s54, v141
	v_med3_f32 v8, v8, s54, v141
	v_med3_f32 v5, v5, s54, v141
	v_med3_f32 v6, v9, s54, v141
	s_waitcnt lgkmcnt(0)
	s_nop 0
	v_cvt_pk_fp8_f32 v11, v16, v14 op_sel:[0,0,1]
	v_cvt_pk_fp8_f32 v2, v4, v5 op_sel:[0,0,1]
	v_cvt_pk_fp8_f32 v3, v8, v6 op_sel:[0,0,1]
	v_add_u32_e32 v4, 0x14c28000, v119
	s_waitcnt lgkmcnt(0)
	buffer_store_dwordx4 v[18:21], v4, s[8:11], 0 offen nt sc1
	ds_write_b64 v124, v[10:11]
	ds_write_b64 v118, v[2:3]
	s_waitcnt lgkmcnt(0)
	ds_read_b128 v[2:5], v140
	s_waitcnt lgkmcnt(0)
	v_add_u32_e32 v6, 0x14c2c000, v119
	s_andn2_b64 vcc, exec, s[12:13]
	s_mov_b64 s[12:13], -1
	s_waitcnt lgkmcnt(0)
	buffer_store_dwordx4 v[2:5], v6, s[8:11], 0 offen nt sc1
	s_cbranch_vccnz .LBB0_1722
	s_andn2_b64 vcc, exec, s[4:5]
	s_cbranch_vccnz .LBB0_1721
	s_barrier
	s_branch .LBB0_1721

; __global__ void __launch_bounds__(NWAVES * 64, 2) mega_fwd(Args args) {
	.amdhsa_kernel _Z8mega_fwd4Args
		.amdhsa_group_segment_fixed_size 0
		.amdhsa_private_segment_fixed_size 0
		.amdhsa_kernarg_size 488
		.amdhsa_user_sgpr_count 2
		.amdhsa_user_sgpr_dispatch_ptr 0
		.amdhsa_user_sgpr_queue_ptr 0
		.amdhsa_user_sgpr_kernarg_segment_ptr 1
		.amdhsa_user_sgpr_dispatch_id 0
		.amdhsa_user_sgpr_kernarg_preload_length 0
		.amdhsa_user_sgpr_kernarg_preload_offset 0
		.amdhsa_user_sgpr_private_segment_size 0
		.amdhsa_uses_dynamic_stack 0
		.amdhsa_enable_private_segment 0
		.amdhsa_system_sgpr_workgroup_id_x 1
		.amdhsa_system_sgpr_workgroup_id_y 0
		.amdhsa_system_sgpr_workgroup_id_z 0
		.amdhsa_system_sgpr_workgroup_info 0
		.amdhsa_system_vgpr_workitem_id 0
		.amdhsa_next_free_vgpr 256
		.amdhsa_next_free_sgpr 102
		.amdhsa_accum_offset 256
		.amdhsa_reserve_vcc 1
		.amdhsa_float_round_mode_32 0
		.amdhsa_float_round_mode_16_64 0
		.amdhsa_float_denorm_mode_32 3
		.amdhsa_float_denorm_mode_16_64 3
		.amdhsa_dx10_clamp 1
		.amdhsa_ieee_mode 1
		.amdhsa_fp16_overflow 0
		.amdhsa_tg_split 0
		.amdhsa_exception_fp_ieee_invalid_op 0
		.amdhsa_exception_fp_denorm_src 0
		.amdhsa_exception_fp_ieee_div_zero 0
		.amdhsa_exception_fp_ieee_overflow 0
		.amdhsa_exception_fp_ieee_underflow 0
		.amdhsa_exception_fp_ieee_inexact 0
		.amdhsa_exception_int_div_zero 0
	.end_amdhsa_kernel

; __global__ void __launch_bounds__(NWAVES * 64, 2) mega_fwd(Args args) {
amdhsa.kernels:
  - .agpr_count:     0
    .args:
      - .offset:         0
        .size:           232
        .value_kind:     by_value
      - .offset:         232
        .size:           4
        .value_kind:     hidden_block_count_x
      - .offset:         236
        .size:           4
        .value_kind:     hidden_block_count_y
      - .offset:         240
        .size:           4
        .value_kind:     hidden_block_count_z
      - .offset:         244
        .size:           2
        .value_kind:     hidden_group_size_x
      - .offset:         246
        .size:           2
        .value_kind:     hidden_group_size_y
      - .offset:         248
        .size:           2
        .value_kind:     hidden_group_size_z
      - .offset:         250
        .size:           2
        .value_kind:     hidden_remainder_x
      - .offset:         252
        .size:           2
        .value_kind:     hidden_remainder_y
      - .offset:         254
        .size:           2
        .value_kind:     hidden_remainder_z
      - .offset:         272
        .size:           8
        .value_kind:     hidden_global_offset_x
      - .offset:         280
        .size:           8
        .value_kind:     hidden_global_offset_y
      - .offset:         288
        .size:           8
        .value_kind:     hidden_global_offset_z
      - .offset:         296
        .size:           2
        .value_kind:     hidden_grid_dims
      - .offset:         352
        .size:           4
        .value_kind:     hidden_dynamic_lds_size
    .group_segment_fixed_size: 0
    .kernarg_segment_align: 8
    .kernarg_segment_size: 488
    .language:       OpenCL C
    .language_version:
      - 2
      - 0
    .max_flat_workgroup_size: 512
    .name:           _Z8mega_fwd4Args
    .private_segment_fixed_size: 0
    .sgpr_count:     108
    .sgpr_spill_count: 22
    .symbol:         _Z8mega_fwd4Args.kd
    .uniform_work_group_size: 1
    .uses_dynamic_stack: false
    .vgpr_count:     256
    .vgpr_spill_count: 0
    .wavefront_size: 64
